# expert GEMM loops: the A-only sub-phases issue their two A-tile DMA loads before the 16 fragment reads
# baseline (speedup 1.0000x reference)
; #define PG8_BWAIT(n) asm volatile("s_waitcnt vmcnt(" #n ")" : "+v"(bv[0]), "+v"(bv[1]), "+v"(bv[2]), "+v"(bv[3]), "+v"(bv[4]), "+v"(bv[5]), "+v"(bv[6]), "+v"(bv[7]) :: "memory")
; #define PG8_STAGE_A(bufoff, V0, V1, kb) do { \
;         __builtin_amdgcn_global_load_lds((const unsigned*)((Abase + (kb)) + (V0)), (LAS unsigned*)(lds + (bufoff) + ldsw), 16, 0, 0); \
;         __builtin_amdgcn_global_load_lds((const unsigned*)((Abase + (kb)) + (V1)), (LAS unsigned*)(lds + (bufoff) + ldsw + 8192), 16, 0, 0); } while (0)
; #define PG8_LDA(dst, b, h) do { _Pragma("unroll") for (int m = 0; m < 4; ++m) _Pragma("unroll") for (int k = 0; k < 2; ++k) dst[m][k] = *(const LAS bf16x8*)(lds + PG8_SA(b, h) + aoff + m * 2048 + k * 1024); } while (0)
; #define PG8_LDB(dst, b, h) do { _Pragma("unroll") for (int n = 0; n < 2; ++n) _Pragma("unroll") for (int k = 0; k < 2; ++k) dst[n][k] = *(const LAS bf16x8*)(lds + PG8_SB(b, h) + boff + n * 2048 + k * 1024); } while (0)
; #define PG8_MMA(ai, bj, At, Bt) do { __builtin_amdgcn_s_setprio(1); _Pragma("unroll") for (int m = 0; m < 4; ++m) _Pragma("unroll") for (int n = 0; n < 2; ++n) _Pragma("unroll") for (int k = 0; k < 2; ++k) \
;         acc[ai][bj][m][n] = __builtin_amdgcn_mfma_f32_16x16x32_bf16(Bt[n][k], At[m][k], acc[ai][bj][m][n], 0, 0, 0); __builtin_amdgcn_s_setprio(0); } while (0)
; #define PG8_WAIT_V(n) asm volatile("s_waitcnt vmcnt(" #n ")" ::: "memory")
; #define PG8_WAIT_L(n) asm volatile("s_waitcnt lgkmcnt(" #n ")" ::: "memory")
; #define PG8_BAR __builtin_amdgcn_s_barrier()
; #define PG8_SCHED __builtin_amdgcn_sched_barrier(0)
; template <class Epi, class Sched, bool ALIGN_EPI>
; __device__ __forceinline__ void gemm_phase(LAS unsigned char* lds, const Gemm g, const Sched& S, const Epi& E) {
;     ...
;             PG8_LDB(B0, 0, 0); PG8_LDB(B1, 0, 1); PG8_SCHED; PG8_LDA(At, 0, 0); PG8_STAGE_A(PG8_SA(1, 1), vc10, vc11, kb1);
;             PG8_WAIT_V(12); PG8_WAIT_L(0); PG8_BAR; PG8_MMA(0, 0, At, B0); PG8_MMA(0, 1, At, B1); PG8_BAR; PG8_SCHED;
;             if (last) { vc10 = vn10; vc11 = vn11; }
;             PG8_BWAIT(2); PG8_BCOMMIT(0); PG8_SCHED; PG8_LDA(At, 0, 1); PG8_BISSUE(t + 3 >= nt ? pbn + (size_t)(t + 3 - nt) * 64 * Sched::LDN : pbc + (size_t)(t + 3) * 64 * Sched::LDN); PG8_STAGE_A(PG8_SA(0, 0), vc00, vc01, kb2);
.LBB0_2251:
	s_add_i32 s54, s53, 2
	s_add_i32 m0, s40, 0xc000
	s_add_u32 s4, s90, s22
	s_addc_u32 s5, s91, s23
	global_load_lds_dwordx4 v234, s[4:5]
	s_add_i32 m0, s40, 0xe000
	s_nop 0
	global_load_lds_dwordx4 v235, s[4:5]
	v_add_u32_e32 v162, 0x10000, v240
	v_add_u32_e32 v174, 0x14000, v240
	ds_read_b128 v[178:181], v162
	ds_read_b128 v[182:185], v162 offset:1024
	ds_read_b128 v[186:189], v162 offset:2048
	ds_read_b128 v[190:193], v162 offset:3072
	ds_read_b128 v[162:165], v174
	ds_read_b128 v[166:169], v174 offset:1024
	ds_read_b128 v[170:173], v174 offset:2048
	ds_read_b128 v[174:177], v174 offset:3072
	s_waitcnt lgkmcnt(0)
	ds_read_b128 v[194:197], v241
	ds_read_b128 v[198:201], v241 offset:1024
	ds_read_b128 v[202:205], v241 offset:2048
	ds_read_b128 v[206:209], v241 offset:3072
	ds_read_b128 v[210:213], v241 offset:4096
	ds_read_b128 v[214:217], v241 offset:5120
	ds_read_b128 v[218:221], v241 offset:6144
	ds_read_b128 v[222:225], v241 offset:7168
	s_waitcnt vmcnt(12)
	s_waitcnt lgkmcnt(0)
	s_barrier
	s_setprio 1
	s_waitcnt lgkmcnt(0)
	v_mfma_f32_16x16x32_bf16 v[158:161], v[178:181], v[194:197], v[158:161]
	v_mfma_f32_16x16x32_bf16 v[150:153], v[186:189], v[194:197], v[150:153]
	v_mfma_f32_16x16x32_bf16 v[142:145], v[178:181], v[202:205], v[142:145]
	v_mfma_f32_16x16x32_bf16 v[134:137], v[186:189], v[202:205], v[134:137]
	v_mfma_f32_16x16x32_bf16 v[126:129], v[178:181], v[210:213], v[126:129]
	v_mfma_f32_16x16x32_bf16 v[118:121], v[186:189], v[210:213], v[118:121]
	v_mfma_f32_16x16x32_bf16 v[110:113], v[178:181], v[218:221], v[110:113]
	v_mfma_f32_16x16x32_bf16 v[102:105], v[186:189], v[218:221], v[102:105]
	v_mfma_f32_16x16x32_bf16 v[158:161], v[182:185], v[198:201], v[158:161]
	v_mfma_f32_16x16x32_bf16 v[150:153], v[190:193], v[198:201], v[150:153]
	v_mfma_f32_16x16x32_bf16 v[142:145], v[182:185], v[206:209], v[142:145]
	v_mfma_f32_16x16x32_bf16 v[134:137], v[190:193], v[206:209], v[134:137]
	v_mfma_f32_16x16x32_bf16 v[126:129], v[182:185], v[214:217], v[126:129]
	v_mfma_f32_16x16x32_bf16 v[118:121], v[190:193], v[214:217], v[118:121]
	v_mfma_f32_16x16x32_bf16 v[110:113], v[182:185], v[222:225], v[110:113]
	v_mfma_f32_16x16x32_bf16 v[102:105], v[190:193], v[222:225], v[102:105]
	s_setprio 0
	s_setprio 1
	v_mfma_f32_16x16x32_bf16 v[154:157], v[162:165], v[194:197], v[154:157]
	v_mfma_f32_16x16x32_bf16 v[146:149], v[170:173], v[194:197], v[146:149]
	v_mfma_f32_16x16x32_bf16 v[138:141], v[162:165], v[202:205], v[138:141]
	v_mfma_f32_16x16x32_bf16 v[130:133], v[170:173], v[202:205], v[130:133]
	v_mfma_f32_16x16x32_bf16 v[122:125], v[162:165], v[210:213], v[122:125]
	v_mfma_f32_16x16x32_bf16 v[114:117], v[170:173], v[210:213], v[114:117]
	v_mfma_f32_16x16x32_bf16 v[106:109], v[162:165], v[218:221], v[106:109]
	v_mfma_f32_16x16x32_bf16 v[98:101], v[170:173], v[218:221], v[98:101]
	v_mfma_f32_16x16x32_bf16 v[154:157], v[166:169], v[198:201], v[154:157]
	v_mfma_f32_16x16x32_bf16 v[146:149], v[174:177], v[198:201], v[146:149]
	v_mfma_f32_16x16x32_bf16 v[138:141], v[166:169], v[206:209], v[138:141]
	v_mfma_f32_16x16x32_bf16 v[130:133], v[174:177], v[206:209], v[130:133]
	v_mfma_f32_16x16x32_bf16 v[122:125], v[166:169], v[214:217], v[122:125]
	v_mfma_f32_16x16x32_bf16 v[114:117], v[174:177], v[214:217], v[114:117]
	v_mfma_f32_16x16x32_bf16 v[106:109], v[166:169], v[222:225], v[106:109]
	v_mfma_f32_16x16x32_bf16 v[98:101], v[174:177], v[222:225], v[98:101]
	s_setprio 0
	s_barrier
	s_waitcnt vmcnt(2)
	s_nop 0
	v_add_u32_e32 v210, 0x10000, v232
	v_cvt_pk_bf16_f32 v194, v2, v6
	v_cvt_pk_bf16_f32 v195, v10, v14
	v_cvt_pk_bf16_f32 v196, v18, v22
	v_cvt_pk_bf16_f32 v197, v26, v30
	v_cvt_pk_bf16_f32 v198, v3, v7
	v_cvt_pk_bf16_f32 v199, v11, v15
	v_cvt_pk_bf16_f32 v200, v19, v23
	v_cvt_pk_bf16_f32 v201, v27, v31
	v_cvt_pk_bf16_f32 v202, v4, v8
	v_cvt_pk_bf16_f32 v203, v12, v16
	v_cvt_pk_bf16_f32 v204, v20, v24
	v_cvt_pk_bf16_f32 v205, v28, v32
	v_cvt_pk_bf16_f32 v206, v5, v9
	v_cvt_pk_bf16_f32 v207, v13, v17
	v_cvt_pk_bf16_f32 v208, v21, v25
	v_cvt_pk_bf16_f32 v209, v29, v33
	v_xor_b32_e32 v211, 64, v210
	v_xor_b32_e32 v212, 0x80, v210
	v_xor_b32_e32 v213, 0xc0, v210
	s_cmp_lt_u32 s54, 13
	s_mov_b64 s[6:7], -1
	s_cbranch_scc0 .LBB0_2253
	s_add_u32 s4, s20, 0x30000
	s_addc_u32 s5, s21, 0
	s_mov_b64 s[6:7], 0

; #define PG8_BWAIT(n) asm volatile("s_waitcnt vmcnt(" #n ")" : "+v"(bv[0]), "+v"(bv[1]), "+v"(bv[2]), "+v"(bv[3]), "+v"(bv[4]), "+v"(bv[5]), "+v"(bv[6]), "+v"(bv[7]) :: "memory")
; #define PG8_STAGE_A(bufoff, V0, V1, kb) do { \
;         __builtin_amdgcn_global_load_lds((const unsigned*)((Abase + (kb)) + (V0)), (LAS unsigned*)(lds + (bufoff) + ldsw), 16, 0, 0); \
;         __builtin_amdgcn_global_load_lds((const unsigned*)((Abase + (kb)) + (V1)), (LAS unsigned*)(lds + (bufoff) + ldsw + 8192), 16, 0, 0); } while (0)
; #define PG8_LDA(dst, b, h) do { _Pragma("unroll") for (int m = 0; m < 4; ++m) _Pragma("unroll") for (int k = 0; k < 2; ++k) dst[m][k] = *(const LAS bf16x8*)(lds + PG8_SA(b, h) + aoff + m * 2048 + k * 1024); } while (0)
; #define PG8_LDB(dst, b, h) do { _Pragma("unroll") for (int n = 0; n < 2; ++n) _Pragma("unroll") for (int k = 0; k < 2; ++k) dst[n][k] = *(const LAS bf16x8*)(lds + PG8_SB(b, h) + boff + n * 2048 + k * 1024); } while (0)
; #define PG8_MMA(ai, bj, At, Bt) do { __builtin_amdgcn_s_setprio(1); _Pragma("unroll") for (int m = 0; m < 4; ++m) _Pragma("unroll") for (int n = 0; n < 2; ++n) _Pragma("unroll") for (int k = 0; k < 2; ++k) \
;         acc[ai][bj][m][n] = __builtin_amdgcn_mfma_f32_16x16x32_bf16(Bt[n][k], At[m][k], acc[ai][bj][m][n], 0, 0, 0); __builtin_amdgcn_s_setprio(0); } while (0)
; #define PG8_WAIT_V(n) asm volatile("s_waitcnt vmcnt(" #n ")" ::: "memory")
; #define PG8_WAIT_L(n) asm volatile("s_waitcnt lgkmcnt(" #n ")" ::: "memory")
; #define PG8_BAR __builtin_amdgcn_s_barrier()
; #define PG8_SCHED __builtin_amdgcn_sched_barrier(0)
; template <class Epi, class Sched, bool ALIGN_EPI>
; __device__ __forceinline__ void gemm_phase(LAS unsigned char* lds, const Gemm g, const Sched& S, const Epi& E) {
;     ...
;             PG8_LDB(B0, 1, 0); PG8_LDB(B1, 1, 1); PG8_SCHED; PG8_LDA(At, 1, 0); PG8_STAGE_A(PG8_SA(0, 1), vc10, vc11, kb2);
;             PG8_WAIT_V(12); PG8_WAIT_L(0); PG8_BAR; PG8_MMA(0, 0, At, B0); PG8_MMA(0, 1, At, B1); PG8_BAR; PG8_SCHED;
;             PG8_BWAIT(2); PG8_BCOMMIT(1); PG8_SCHED; PG8_LDA(At, 1, 1); PG8_BISSUE(t + 4 >= nt ? pbn + (size_t)(t + 4 - nt) * 64 * Sched::LDN : pbc + (size_t)(t + 4) * 64 * Sched::LDN); PG8_STAGE_A(PG8_SA(1, 0), vc00, vc01, kb2 + 128u);
.LBB0_2257:
	v_cndmask_b32_e64 v235, v235, v245, s[6:7]
	v_cndmask_b32_e64 v234, v234, v244, s[6:7]
	s_barrier
	s_mov_b32 m0, s42
	s_nop 0
	global_load_lds_dwordx4 v234, s[26:27]
	s_mov_b32 m0, s43
	s_nop 0
	global_load_lds_dwordx4 v235, s[26:27]
	v_add_u32_e32 v162, 0x18000, v240
	v_add_u32_e32 v174, 0x1c000, v240
	ds_read_b128 v[178:181], v162
	ds_read_b128 v[182:185], v162 offset:1024
	ds_read_b128 v[186:189], v162 offset:2048
	ds_read_b128 v[190:193], v162 offset:3072
	ds_read_b128 v[162:165], v174
	ds_read_b128 v[166:169], v174 offset:1024
	ds_read_b128 v[170:173], v174 offset:2048
	ds_read_b128 v[174:177], v174 offset:3072
	s_waitcnt lgkmcnt(0)
	ds_read_b128 v[194:197], v241 offset:32768
	ds_read_b128 v[198:201], v241 offset:33792
	ds_read_b128 v[202:205], v241 offset:34816
	ds_read_b128 v[206:209], v241 offset:35840
	ds_read_b128 v[210:213], v241 offset:36864
	ds_read_b128 v[214:217], v241 offset:37888
	ds_read_b128 v[218:221], v241 offset:38912
	ds_read_b128 v[222:225], v241 offset:39936
	s_waitcnt vmcnt(12)
	s_waitcnt lgkmcnt(0)
	s_barrier
	s_setprio 1
	s_waitcnt lgkmcnt(0)
	v_mfma_f32_16x16x32_bf16 v[158:161], v[178:181], v[194:197], v[158:161]
	v_mfma_f32_16x16x32_bf16 v[150:153], v[186:189], v[194:197], v[150:153]
	v_mfma_f32_16x16x32_bf16 v[142:145], v[178:181], v[202:205], v[142:145]
	v_mfma_f32_16x16x32_bf16 v[134:137], v[186:189], v[202:205], v[134:137]
	v_mfma_f32_16x16x32_bf16 v[126:129], v[178:181], v[210:213], v[126:129]
	v_mfma_f32_16x16x32_bf16 v[118:121], v[186:189], v[210:213], v[118:121]
	v_mfma_f32_16x16x32_bf16 v[110:113], v[178:181], v[218:221], v[110:113]
	v_mfma_f32_16x16x32_bf16 v[102:105], v[186:189], v[218:221], v[102:105]
	v_mfma_f32_16x16x32_bf16 v[158:161], v[182:185], v[198:201], v[158:161]
	v_mfma_f32_16x16x32_bf16 v[150:153], v[190:193], v[198:201], v[150:153]
	v_mfma_f32_16x16x32_bf16 v[142:145], v[182:185], v[206:209], v[142:145]
	v_mfma_f32_16x16x32_bf16 v[134:137], v[190:193], v[206:209], v[134:137]
	v_mfma_f32_16x16x32_bf16 v[126:129], v[182:185], v[214:217], v[126:129]
	v_mfma_f32_16x16x32_bf16 v[118:121], v[190:193], v[214:217], v[118:121]
	v_mfma_f32_16x16x32_bf16 v[110:113], v[182:185], v[222:225], v[110:113]
	v_mfma_f32_16x16x32_bf16 v[102:105], v[190:193], v[222:225], v[102:105]
	s_setprio 0
	s_setprio 1
	v_mfma_f32_16x16x32_bf16 v[154:157], v[162:165], v[194:197], v[154:157]
	v_mfma_f32_16x16x32_bf16 v[146:149], v[170:173], v[194:197], v[146:149]
	v_mfma_f32_16x16x32_bf16 v[138:141], v[162:165], v[202:205], v[138:141]
	v_mfma_f32_16x16x32_bf16 v[130:133], v[170:173], v[202:205], v[130:133]
	v_mfma_f32_16x16x32_bf16 v[122:125], v[162:165], v[210:213], v[122:125]
	v_mfma_f32_16x16x32_bf16 v[114:117], v[170:173], v[210:213], v[114:117]
	v_mfma_f32_16x16x32_bf16 v[106:109], v[162:165], v[218:221], v[106:109]
	v_mfma_f32_16x16x32_bf16 v[98:101], v[170:173], v[218:221], v[98:101]
	v_mfma_f32_16x16x32_bf16 v[154:157], v[166:169], v[198:201], v[154:157]
	v_mfma_f32_16x16x32_bf16 v[146:149], v[174:177], v[198:201], v[146:149]
	v_mfma_f32_16x16x32_bf16 v[138:141], v[166:169], v[206:209], v[138:141]
	v_mfma_f32_16x16x32_bf16 v[130:133], v[174:177], v[206:209], v[130:133]
	v_mfma_f32_16x16x32_bf16 v[122:125], v[166:169], v[214:217], v[122:125]
	v_mfma_f32_16x16x32_bf16 v[114:117], v[174:177], v[214:217], v[114:117]
	v_mfma_f32_16x16x32_bf16 v[106:109], v[166:169], v[222:225], v[106:109]
	v_mfma_f32_16x16x32_bf16 v[98:101], v[174:177], v[222:225], v[98:101]
	s_setprio 0
	s_barrier
	s_waitcnt vmcnt(2)
	s_nop 0
	v_add_u32_e32 v210, 0x18000, v232
	v_cvt_pk_bf16_f32 v194, v2, v6
	v_cvt_pk_bf16_f32 v195, v10, v14
	v_cvt_pk_bf16_f32 v196, v18, v22
	v_cvt_pk_bf16_f32 v197, v26, v30
	v_cvt_pk_bf16_f32 v198, v3, v7
	v_cvt_pk_bf16_f32 v199, v11, v15
	v_cvt_pk_bf16_f32 v200, v19, v23
	v_cvt_pk_bf16_f32 v201, v27, v31
	v_cvt_pk_bf16_f32 v202, v4, v8
	v_cvt_pk_bf16_f32 v203, v12, v16
	v_cvt_pk_bf16_f32 v204, v20, v24
	v_cvt_pk_bf16_f32 v205, v28, v32
	v_cvt_pk_bf16_f32 v206, v5, v9
	v_cvt_pk_bf16_f32 v207, v13, v17
	v_cvt_pk_bf16_f32 v208, v21, v25
	v_cvt_pk_bf16_f32 v209, v29, v33
	v_xor_b32_e32 v211, 64, v210
	v_xor_b32_e32 v212, 0x80, v210
	v_xor_b32_e32 v213, 0xc0, v210
	s_cmp_lt_u32 s54, 12
	s_mov_b64 s[28:29], -1
	s_cbranch_scc0 .LBB0_2259
	s_add_u32 s6, s20, 0x40000
	s_addc_u32 s7, s21, 0
	s_mov_b64 s[28:29], 0

; #define PG8_BWAIT(n) asm volatile("s_waitcnt vmcnt(" #n ")" : "+v"(bv[0]), "+v"(bv[1]), "+v"(bv[2]), "+v"(bv[3]), "+v"(bv[4]), "+v"(bv[5]), "+v"(bv[6]), "+v"(bv[7]) :: "memory")
; #define PG8_STAGE_A(bufoff, V0, V1, kb) do { \
;         __builtin_amdgcn_global_load_lds((const unsigned*)((Abase + (kb)) + (V0)), (LAS unsigned*)(lds + (bufoff) + ldsw), 16, 0, 0); \
;         __builtin_amdgcn_global_load_lds((const unsigned*)((Abase + (kb)) + (V1)), (LAS unsigned*)(lds + (bufoff) + ldsw + 8192), 16, 0, 0); } while (0)
; #define PG8_LDA(dst, b, h) do { _Pragma("unroll") for (int m = 0; m < 4; ++m) _Pragma("unroll") for (int k = 0; k < 2; ++k) dst[m][k] = *(const LAS bf16x8*)(lds + PG8_SA(b, h) + aoff + m * 2048 + k * 1024); } while (0)
; #define PG8_LDB(dst, b, h) do { _Pragma("unroll") for (int n = 0; n < 2; ++n) _Pragma("unroll") for (int k = 0; k < 2; ++k) dst[n][k] = *(const LAS bf16x8*)(lds + PG8_SB(b, h) + boff + n * 2048 + k * 1024); } while (0)
; #define PG8_MMA(ai, bj, At, Bt) do { __builtin_amdgcn_s_setprio(1); _Pragma("unroll") for (int m = 0; m < 4; ++m) _Pragma("unroll") for (int n = 0; n < 2; ++n) _Pragma("unroll") for (int k = 0; k < 2; ++k) \
;         acc[ai][bj][m][n] = __builtin_amdgcn_mfma_f32_16x16x32_bf16(Bt[n][k], At[m][k], acc[ai][bj][m][n], 0, 0, 0); __builtin_amdgcn_s_setprio(0); } while (0)
; #define PG8_WAIT_V(n) asm volatile("s_waitcnt vmcnt(" #n ")" ::: "memory")
; #define PG8_WAIT_L(n) asm volatile("s_waitcnt lgkmcnt(" #n ")" ::: "memory")
; #define PG8_BAR __builtin_amdgcn_s_barrier()
; template <class Epi, class Sched, bool ALIGN_EPI>
; __device__ __forceinline__ void gemm_phase(LAS unsigned char* lds, const Gemm g, const Sched& S, const Epi& E) {
;     ...
;             PG8_LDB(B0, 0, 0); PG8_LDB(B1, 0, 1); PG8_SCHED; PG8_LDA(At, 0, 0); PG8_STAGE_A(PG8_SA(1, 1), vc10, vc11, kb1);
;             PG8_WAIT_V(12); PG8_WAIT_L(0); PG8_BAR; PG8_MMA(0, 0, At, B0); PG8_MMA(0, 1, At, B1); PG8_BAR; PG8_SCHED;
;             if (last) { vc10 = vn10; vc11 = vn11; }
;             PG8_BWAIT(2); PG8_BCOMMIT(0); PG8_SCHED; PG8_LDA(At, 0, 1); PG8_BISSUE(t + 3 >= nt ? pbn + (size_t)(t + 3 - nt) * 64 * Sched::LDN : pbc + (size_t)(t + 3) * 64 * Sched::LDN); PG8_STAGE_A(PG8_SA(0, 0), vc00, vc01, kb2);
;             PG8_WAIT_V(12); PG8_WAIT_L(0); PG8_BAR; if (half1) { PG8_MMA(1, 0, At, B0); PG8_MMA(1, 1, At, B1); } PG8_BAR; PG8_SCHED;
.LBB0_2448:
	s_lshl_b32 s5, s50, 7
	s_add_i32 s4, s5, 0x100
	v_cndmask_b32_e64 v228, v228, v250, s[28:29]
	v_readlane_b32 s54, v254, 53
	v_readlane_b32 s55, v254, 54
	s_add_u32 s30, s54, s5
	s_addc_u32 s31, s55, 0
	v_lshl_add_u64 v[236:237], s[30:31], 0, v[230:231]
	v_lshl_add_u64 v[236:237], v[236:237], 0, s[16:17]
	s_add_i32 m0, s35, 0xc000
	v_mov_b32_e32 v233, v231
	global_load_lds_dwordx4 v[236:237], off
	v_lshl_add_u64 v[236:237], s[30:31], 0, v[232:233]
	v_lshl_add_u64 v[236:237], v[236:237], 0, s[16:17]
	s_add_i32 m0, s35, 0xe000
	s_nop 0
	global_load_lds_dwordx4 v[236:237], off
	v_add_u32_e32 v162, 0x10000, v247
	v_add_u32_e32 v174, 0x14000, v247
	ds_read_b128 v[178:181], v162
	ds_read_b128 v[182:185], v162 offset:1024
	ds_read_b128 v[186:189], v162 offset:2048
	ds_read_b128 v[190:193], v162 offset:3072
	ds_read_b128 v[162:165], v174
	ds_read_b128 v[166:169], v174 offset:1024
	ds_read_b128 v[170:173], v174 offset:2048
	ds_read_b128 v[174:177], v174 offset:3072
	s_waitcnt lgkmcnt(0)
	ds_read_b128 v[194:197], v248
	ds_read_b128 v[198:201], v248 offset:1024
	ds_read_b128 v[202:205], v248 offset:2048
	ds_read_b128 v[206:209], v248 offset:3072
	ds_read_b128 v[210:213], v248 offset:4096
	ds_read_b128 v[214:217], v248 offset:5120
	ds_read_b128 v[218:221], v248 offset:6144
	ds_read_b128 v[222:225], v248 offset:7168
	s_waitcnt vmcnt(12)
	s_waitcnt lgkmcnt(0)
	s_barrier
	s_setprio 1
	s_waitcnt lgkmcnt(0)
	v_mfma_f32_16x16x32_bf16 v[158:161], v[178:181], v[194:197], v[158:161]
	v_mfma_f32_16x16x32_bf16 v[154:157], v[186:189], v[194:197], v[154:157]
	v_mfma_f32_16x16x32_bf16 v[142:145], v[178:181], v[202:205], v[142:145]
	v_mfma_f32_16x16x32_bf16 v[138:141], v[186:189], v[202:205], v[138:141]
	v_mfma_f32_16x16x32_bf16 v[126:129], v[178:181], v[210:213], v[126:129]
	v_mfma_f32_16x16x32_bf16 v[122:125], v[186:189], v[210:213], v[122:125]
	v_mfma_f32_16x16x32_bf16 v[110:113], v[178:181], v[218:221], v[110:113]
	v_mfma_f32_16x16x32_bf16 v[106:109], v[186:189], v[218:221], v[106:109]
	v_mfma_f32_16x16x32_bf16 v[158:161], v[182:185], v[198:201], v[158:161]
	v_mfma_f32_16x16x32_bf16 v[154:157], v[190:193], v[198:201], v[154:157]
	v_mfma_f32_16x16x32_bf16 v[142:145], v[182:185], v[206:209], v[142:145]
	v_mfma_f32_16x16x32_bf16 v[138:141], v[190:193], v[206:209], v[138:141]
	v_mfma_f32_16x16x32_bf16 v[126:129], v[182:185], v[214:217], v[126:129]
	v_mfma_f32_16x16x32_bf16 v[122:125], v[190:193], v[214:217], v[122:125]
	v_mfma_f32_16x16x32_bf16 v[110:113], v[182:185], v[222:225], v[110:113]
	v_mfma_f32_16x16x32_bf16 v[106:109], v[190:193], v[222:225], v[106:109]
	s_setprio 0
	s_setprio 1
	v_mfma_f32_16x16x32_bf16 v[150:153], v[162:165], v[194:197], v[150:153]
	v_mfma_f32_16x16x32_bf16 v[146:149], v[170:173], v[194:197], v[146:149]
	v_mfma_f32_16x16x32_bf16 v[134:137], v[162:165], v[202:205], v[134:137]
	v_mfma_f32_16x16x32_bf16 v[130:133], v[170:173], v[202:205], v[130:133]
	v_mfma_f32_16x16x32_bf16 v[118:121], v[162:165], v[210:213], v[118:121]
	v_mfma_f32_16x16x32_bf16 v[114:117], v[170:173], v[210:213], v[114:117]
	v_mfma_f32_16x16x32_bf16 v[102:105], v[162:165], v[218:221], v[102:105]
	v_mfma_f32_16x16x32_bf16 v[98:101], v[170:173], v[218:221], v[98:101]
	v_mfma_f32_16x16x32_bf16 v[150:153], v[166:169], v[198:201], v[150:153]
	v_mfma_f32_16x16x32_bf16 v[146:149], v[174:177], v[198:201], v[146:149]
	v_mfma_f32_16x16x32_bf16 v[134:137], v[166:169], v[206:209], v[134:137]
	v_mfma_f32_16x16x32_bf16 v[130:133], v[174:177], v[206:209], v[130:133]
	v_mfma_f32_16x16x32_bf16 v[118:121], v[166:169], v[214:217], v[118:121]
	v_mfma_f32_16x16x32_bf16 v[114:117], v[174:177], v[214:217], v[114:117]
	v_mfma_f32_16x16x32_bf16 v[102:105], v[166:169], v[222:225], v[102:105]
	v_mfma_f32_16x16x32_bf16 v[98:101], v[174:177], v[222:225], v[98:101]
	s_setprio 0
	s_barrier
	s_waitcnt vmcnt(2)
	v_cndmask_b32_e64 v226, v226, v249, s[28:29]
	v_add_u32_e32 v210, 0x10000, v242
	v_cvt_pk_bf16_f32 v194, v2, v6
	v_cvt_pk_bf16_f32 v195, v10, v14
	v_cvt_pk_bf16_f32 v196, v18, v22
	v_cvt_pk_bf16_f32 v197, v26, v30
	v_cvt_pk_bf16_f32 v198, v3, v7
	v_cvt_pk_bf16_f32 v199, v11, v15
	v_cvt_pk_bf16_f32 v200, v19, v23
	v_cvt_pk_bf16_f32 v201, v27, v31
	v_cvt_pk_bf16_f32 v202, v4, v8
	v_cvt_pk_bf16_f32 v203, v12, v16
	v_cvt_pk_bf16_f32 v204, v20, v24
	v_cvt_pk_bf16_f32 v205, v28, v32
	v_cvt_pk_bf16_f32 v206, v5, v9
	v_cvt_pk_bf16_f32 v207, v13, v17
	v_cvt_pk_bf16_f32 v208, v21, v25
	v_cvt_pk_bf16_f32 v209, v29, v33
	v_xor_b32_e32 v211, 64, v210
	v_xor_b32_e32 v212, 0x80, v210
	v_xor_b32_e32 v213, 0xc0, v210
	s_add_i32 s10, s50, -1
	s_lshl_b64 s[30:31], s[10:11], 18
	s_add_u32 s5, s47, s30
	s_addc_u32 s10, s21, s31
	s_and_b64 s[30:31], s[26:27], exec
	s_cselect_b32 s30, s48, s5
	s_cselect_b32 s31, s49, s10
	s_add_u32 s52, s30, 0x1000
	global_load_dwordx4 v[2:5], v240, s[30:31] offset:0
	s_addc_u32 s53, s31, 0
	global_load_dwordx4 v[6:9], v240, s[52:53] offset:0
	s_add_u32 s52, s30, 0x2000
	s_addc_u32 s53, s31, 0
	global_load_dwordx4 v[10:13], v240, s[52:53] offset:0
	s_add_u32 s52, s30, 0x3000
	s_addc_u32 s53, s31, 0
	global_load_dwordx4 v[14:17], v240, s[52:53] offset:0
	s_add_u32 s52, s30, 0x4000
	s_addc_u32 s53, s31, 0
	global_load_dwordx4 v[18:21], v240, s[52:53] offset:0
	s_add_u32 s52, s30, 0x5000
	s_addc_u32 s53, s31, 0
	global_load_dwordx4 v[22:25], v240, s[52:53] offset:0
	s_add_u32 s52, s30, 0x6000
	s_addc_u32 s53, s31, 0
	s_add_u32 s30, s30, 0x7000
	global_load_dwordx4 v[26:29], v240, s[52:53] offset:0
	s_addc_u32 s31, s31, 0
	global_load_dwordx4 v[30:33], v240, s[30:31] offset:0
	ds_write_b128 v210, v[194:197]
	ds_write_b128 v211, v[198:201]
	ds_write_b128 v212, v[202:205]
	ds_write_b128 v213, v[206:209]
	ds_read_b128 v[218:221], v248 offset:16384
	ds_read_b128 v[222:225], v248 offset:17408
	ds_read_b128 v[210:213], v248 offset:18432
	ds_read_b128 v[214:217], v248 offset:19456
	ds_read_b128 v[202:205], v248 offset:20480
	ds_read_b128 v[206:209], v248 offset:21504
	ds_read_b128 v[194:197], v248 offset:22528
	ds_read_b128 v[198:201], v248 offset:23552
	s_and_b64 s[30:31], s[28:29], exec
	s_cselect_b32 s4, 0, s4
	s_cselect_b32 s5, 0, 0
	s_add_u32 s30, s54, s4
	s_mov_b32 m0, s35
	s_addc_u32 s31, s55, s5
	global_load_lds_dwordx4 v226, s[30:31]
	s_mov_b32 m0, s36
	v_mov_b32_e32 v227, v231
	global_load_lds_dwordx4 v228, s[30:31]
	s_waitcnt vmcnt(12)
	s_waitcnt lgkmcnt(0)
	v_lshl_add_u64 v[238:239], s[30:31], 0, v[226:227]
	v_mov_b32_e32 v229, v231
	v_cndmask_b32_e64 v227, 0, 1, s[24:25]
	v_lshl_add_u64 v[236:237], s[30:31], 0, v[228:229]
	v_cmp_ne_u32_e64 s[4:5], 1, v227
	s_andn2_b64 vcc, exec, s[24:25]
	s_barrier
; #define PG8_STAGE_A(bufoff, V0, V1, kb) do { \
;         __builtin_amdgcn_global_load_lds((const unsigned*)((Abase + (kb)) + (V0)), (LAS unsigned*)(lds + (bufoff) + ldsw), 16, 0, 0); \
;         __builtin_amdgcn_global_load_lds((const unsigned*)((Abase + (kb)) + (V1)), (LAS unsigned*)(lds + (bufoff) + ldsw + 8192), 16, 0, 0); } while (0)
; #define PG8_LDA(dst, b, h) do { _Pragma("unroll") for (int m = 0; m < 4; ++m) _Pragma("unroll") for (int k = 0; k < 2; ++k) dst[m][k] = *(const LAS bf16x8*)(lds + PG8_SA(b, h) + aoff + m * 2048 + k * 1024); } while (0)
; #define PG8_LDB(dst, b, h) do { _Pragma("unroll") for (int n = 0; n < 2; ++n) _Pragma("unroll") for (int k = 0; k < 2; ++k) dst[n][k] = *(const LAS bf16x8*)(lds + PG8_SB(b, h) + boff + n * 2048 + k * 1024); } while (0)
; #define PG8_MMA(ai, bj, At, Bt) do { __builtin_amdgcn_s_setprio(1); _Pragma("unroll") for (int m = 0; m < 4; ++m) _Pragma("unroll") for (int n = 0; n < 2; ++n) _Pragma("unroll") for (int k = 0; k < 2; ++k) \
;         acc[ai][bj][m][n] = __builtin_amdgcn_mfma_f32_16x16x32_bf16(Bt[n][k], At[m][k], acc[ai][bj][m][n], 0, 0, 0); __builtin_amdgcn_s_setprio(0); } while (0)
; #define PG8_WAIT_V(n) asm volatile("s_waitcnt vmcnt(" #n ")" ::: "memory")
; #define PG8_WAIT_L(n) asm volatile("s_waitcnt lgkmcnt(" #n ")" ::: "memory")
; #define PG8_BAR __builtin_amdgcn_s_barrier()
; #define PG8_SCHED __builtin_amdgcn_sched_barrier(0)
; template <class Epi, class Sched, bool ALIGN_EPI>
; __device__ __forceinline__ void gemm_phase(LAS unsigned char* lds, const Gemm g, const Sched& S, const Epi& E) {
;     ...
;             PG8_WAIT_V(12); PG8_WAIT_L(0); PG8_BAR; if (half1) { PG8_MMA(1, 0, At, B0); PG8_MMA(1, 1, At, B1); } PG8_BAR; PG8_SCHED;
;             PG8_LDB(B0, 1, 0); PG8_LDB(B1, 1, 1); PG8_SCHED; PG8_LDA(At, 1, 0); PG8_STAGE_A(PG8_SA(0, 1), vc10, vc11, kb2);
;             PG8_WAIT_V(12); PG8_WAIT_L(0); PG8_BAR; PG8_MMA(0, 0, At, B0); PG8_MMA(0, 1, At, B1); PG8_BAR; PG8_SCHED;
	s_cbranch_vccnz .LBB0_2450
	s_setprio 1
	s_waitcnt lgkmcnt(0)
	v_mfma_f32_16x16x32_bf16 v[94:97], v[178:181], v[218:221], v[94:97]
	v_mfma_f32_16x16x32_bf16 v[90:93], v[186:189], v[218:221], v[90:93]
	v_mfma_f32_16x16x32_bf16 v[78:81], v[178:181], v[210:213], v[78:81]
	v_mfma_f32_16x16x32_bf16 v[74:77], v[186:189], v[210:213], v[74:77]
	v_mfma_f32_16x16x32_bf16 v[62:65], v[178:181], v[202:205], v[62:65]
	v_mfma_f32_16x16x32_bf16 v[58:61], v[186:189], v[202:205], v[58:61]
	v_mfma_f32_16x16x32_bf16 v[46:49], v[178:181], v[194:197], v[46:49]
	v_mfma_f32_16x16x32_bf16 v[42:45], v[186:189], v[194:197], v[42:45]
	v_mfma_f32_16x16x32_bf16 v[94:97], v[182:185], v[222:225], v[94:97]
	v_mfma_f32_16x16x32_bf16 v[90:93], v[190:193], v[222:225], v[90:93]
	v_mfma_f32_16x16x32_bf16 v[78:81], v[182:185], v[214:217], v[78:81]
	v_mfma_f32_16x16x32_bf16 v[74:77], v[190:193], v[214:217], v[74:77]
	v_mfma_f32_16x16x32_bf16 v[62:65], v[182:185], v[206:209], v[62:65]
	v_mfma_f32_16x16x32_bf16 v[58:61], v[190:193], v[206:209], v[58:61]
	v_mfma_f32_16x16x32_bf16 v[46:49], v[182:185], v[198:201], v[46:49]
	v_mfma_f32_16x16x32_bf16 v[42:45], v[190:193], v[198:201], v[42:45]
	s_setprio 0
	s_setprio 1
	v_mfma_f32_16x16x32_bf16 v[86:89], v[162:165], v[218:221], v[86:89]
	v_mfma_f32_16x16x32_bf16 v[82:85], v[170:173], v[218:221], v[82:85]
	v_mfma_f32_16x16x32_bf16 v[70:73], v[162:165], v[210:213], v[70:73]
	v_mfma_f32_16x16x32_bf16 v[66:69], v[170:173], v[210:213], v[66:69]
	v_mfma_f32_16x16x32_bf16 v[54:57], v[162:165], v[202:205], v[54:57]
	v_mfma_f32_16x16x32_bf16 v[50:53], v[170:173], v[202:205], v[50:53]
	v_mfma_f32_16x16x32_bf16 v[38:41], v[162:165], v[194:197], v[38:41]
	v_mfma_f32_16x16x32_bf16 v[34:37], v[170:173], v[194:197], v[34:37]
	v_mfma_f32_16x16x32_bf16 v[86:89], v[166:169], v[222:225], v[86:89]
	v_mfma_f32_16x16x32_bf16 v[82:85], v[174:177], v[222:225], v[82:85]
	v_mfma_f32_16x16x32_bf16 v[70:73], v[166:169], v[214:217], v[70:73]
	v_mfma_f32_16x16x32_bf16 v[66:69], v[174:177], v[214:217], v[66:69]
	v_mfma_f32_16x16x32_bf16 v[54:57], v[166:169], v[206:209], v[54:57]
	v_mfma_f32_16x16x32_bf16 v[50:53], v[174:177], v[206:209], v[50:53]
	v_mfma_f32_16x16x32_bf16 v[38:41], v[166:169], v[198:201], v[38:41]
	v_mfma_f32_16x16x32_bf16 v[34:37], v[174:177], v[198:201], v[34:37]
	s_setprio 0
.LBB0_2450:
	v_cndmask_b32_e64 v232, v232, v252, s[28:29]
	v_cndmask_b32_e64 v230, v230, v251, s[28:29]
	s_barrier
	s_mov_b32 m0, s37
	s_nop 0
	global_load_lds_dwordx4 v230, s[30:31]
	s_mov_b32 m0, s38
	s_nop 0
	global_load_lds_dwordx4 v232, s[30:31]
	v_add_u32_e32 v162, 0x18000, v247
	v_add_u32_e32 v174, 0x1c000, v247
	ds_read_b128 v[178:181], v162
	ds_read_b128 v[182:185], v162 offset:1024
	ds_read_b128 v[186:189], v162 offset:2048
	ds_read_b128 v[190:193], v162 offset:3072
	ds_read_b128 v[162:165], v174
	ds_read_b128 v[166:169], v174 offset:1024
	ds_read_b128 v[170:173], v174 offset:2048
	ds_read_b128 v[174:177], v174 offset:3072
	s_waitcnt lgkmcnt(0)
	ds_read_b128 v[194:197], v248 offset:32768
	ds_read_b128 v[198:201], v248 offset:33792
	ds_read_b128 v[202:205], v248 offset:34816
	ds_read_b128 v[206:209], v248 offset:35840
	ds_read_b128 v[210:213], v248 offset:36864
	ds_read_b128 v[214:217], v248 offset:37888
	ds_read_b128 v[218:221], v248 offset:38912
	ds_read_b128 v[222:225], v248 offset:39936
	s_waitcnt vmcnt(12)
	s_waitcnt lgkmcnt(0)
	s_barrier
	s_setprio 1
	s_waitcnt lgkmcnt(0)
	v_mfma_f32_16x16x32_bf16 v[158:161], v[178:181], v[194:197], v[158:161]
	v_mfma_f32_16x16x32_bf16 v[154:157], v[186:189], v[194:197], v[154:157]
	v_mfma_f32_16x16x32_bf16 v[142:145], v[178:181], v[202:205], v[142:145]
	v_mfma_f32_16x16x32_bf16 v[138:141], v[186:189], v[202:205], v[138:141]
	v_mfma_f32_16x16x32_bf16 v[126:129], v[178:181], v[210:213], v[126:129]
	v_mfma_f32_16x16x32_bf16 v[122:125], v[186:189], v[210:213], v[122:125]
	v_mfma_f32_16x16x32_bf16 v[110:113], v[178:181], v[218:221], v[110:113]
	v_mfma_f32_16x16x32_bf16 v[106:109], v[186:189], v[218:221], v[106:109]
	v_mfma_f32_16x16x32_bf16 v[158:161], v[182:185], v[198:201], v[158:161]
	v_mfma_f32_16x16x32_bf16 v[154:157], v[190:193], v[198:201], v[154:157]
	v_mfma_f32_16x16x32_bf16 v[142:145], v[182:185], v[206:209], v[142:145]
	v_mfma_f32_16x16x32_bf16 v[138:141], v[190:193], v[206:209], v[138:141]
	v_mfma_f32_16x16x32_bf16 v[126:129], v[182:185], v[214:217], v[126:129]
	v_mfma_f32_16x16x32_bf16 v[122:125], v[190:193], v[214:217], v[122:125]
	v_mfma_f32_16x16x32_bf16 v[110:113], v[182:185], v[222:225], v[110:113]
	v_mfma_f32_16x16x32_bf16 v[106:109], v[190:193], v[222:225], v[106:109]
	s_setprio 0
	s_setprio 1
	v_mfma_f32_16x16x32_bf16 v[150:153], v[162:165], v[194:197], v[150:153]
	v_mfma_f32_16x16x32_bf16 v[146:149], v[170:173], v[194:197], v[146:149]
	v_mfma_f32_16x16x32_bf16 v[134:137], v[162:165], v[202:205], v[134:137]
	v_mfma_f32_16x16x32_bf16 v[130:133], v[170:173], v[202:205], v[130:133]
	v_mfma_f32_16x16x32_bf16 v[118:121], v[162:165], v[210:213], v[118:121]
	v_mfma_f32_16x16x32_bf16 v[114:117], v[170:173], v[210:213], v[114:117]
	v_mfma_f32_16x16x32_bf16 v[102:105], v[162:165], v[218:221], v[102:105]
	v_mfma_f32_16x16x32_bf16 v[98:101], v[170:173], v[218:221], v[98:101]
	v_mfma_f32_16x16x32_bf16 v[150:153], v[166:169], v[198:201], v[150:153]
	v_mfma_f32_16x16x32_bf16 v[146:149], v[174:177], v[198:201], v[146:149]
	v_mfma_f32_16x16x32_bf16 v[134:137], v[166:169], v[206:209], v[134:137]
	v_mfma_f32_16x16x32_bf16 v[130:133], v[174:177], v[206:209], v[130:133]
	v_mfma_f32_16x16x32_bf16 v[118:121], v[166:169], v[214:217], v[118:121]
	v_mfma_f32_16x16x32_bf16 v[114:117], v[174:177], v[214:217], v[114:117]
	v_mfma_f32_16x16x32_bf16 v[102:105], v[166:169], v[222:225], v[102:105]
	v_mfma_f32_16x16x32_bf16 v[98:101], v[174:177], v[222:225], v[98:101]
	s_setprio 0
	s_barrier
; #define PG8_BWAIT(n) asm volatile("s_waitcnt vmcnt(" #n ")" : "+v"(bv[0]), "+v"(bv[1]), "+v"(bv[2]), "+v"(bv[3]), "+v"(bv[4]), "+v"(bv[5]), "+v"(bv[6]), "+v"(bv[7]) :: "memory")
; #define PG8_STAGE_A(bufoff, V0, V1, kb) do { \
;         __builtin_amdgcn_global_load_lds((const unsigned*)((Abase + (kb)) + (V0)), (LAS unsigned*)(lds + (bufoff) + ldsw), 16, 0, 0); \
;         __builtin_amdgcn_global_load_lds((const unsigned*)((Abase + (kb)) + (V1)), (LAS unsigned*)(lds + (bufoff) + ldsw + 8192), 16, 0, 0); } while (0)
; #define PG8_LDA(dst, b, h) do { _Pragma("unroll") for (int m = 0; m < 4; ++m) _Pragma("unroll") for (int k = 0; k < 2; ++k) dst[m][k] = *(const LAS bf16x8*)(lds + PG8_SA(b, h) + aoff + m * 2048 + k * 1024); } while (0)
; #define PG8_MMA(ai, bj, At, Bt) do { __builtin_amdgcn_s_setprio(1); _Pragma("unroll") for (int m = 0; m < 4; ++m) _Pragma("unroll") for (int n = 0; n < 2; ++n) _Pragma("unroll") for (int k = 0; k < 2; ++k) \
;         acc[ai][bj][m][n] = __builtin_amdgcn_mfma_f32_16x16x32_bf16(Bt[n][k], At[m][k], acc[ai][bj][m][n], 0, 0, 0); __builtin_amdgcn_s_setprio(0); } while (0)
; #define PG8_WAIT_V(n) asm volatile("s_waitcnt vmcnt(" #n ")" ::: "memory")
; #define PG8_WAIT_L(n) asm volatile("s_waitcnt lgkmcnt(" #n ")" ::: "memory")
; #define PG8_BAR __builtin_amdgcn_s_barrier()
; #define PG8_SCHED __builtin_amdgcn_sched_barrier(0)
; template <class Epi, class Sched, bool ALIGN_EPI>
; __device__ __forceinline__ void gemm_phase(LAS unsigned char* lds, const Gemm g, const Sched& S, const Epi& E) {
;     ...
;             PG8_BWAIT(2); PG8_BCOMMIT(1); PG8_SCHED; PG8_LDA(At, 1, 1); PG8_BISSUE(t + 4 >= nt ? pbn + (size_t)(t + 4 - nt) * 64 * Sched::LDN : pbc + (size_t)(t + 4) * 64 * Sched::LDN); PG8_STAGE_A(PG8_SA(1, 0), vc00, vc01, kb2 + 128u);
;             PG8_WAIT_V(12); PG8_WAIT_L(0); PG8_BAR; if (half1) { PG8_MMA(1, 0, At, B0); PG8_MMA(1, 1, At, B1); } PG8_BAR; PG8_SCHED;
	s_waitcnt vmcnt(2)
	s_nop 0
	v_add_u32_e32 v210, 0x18000, v242
	v_cvt_pk_bf16_f32 v194, v2, v6
	v_cvt_pk_bf16_f32 v195, v10, v14
	v_cvt_pk_bf16_f32 v196, v18, v22
	v_cvt_pk_bf16_f32 v197, v26, v30
	v_cvt_pk_bf16_f32 v198, v3, v7
	v_cvt_pk_bf16_f32 v199, v11, v15
	v_cvt_pk_bf16_f32 v200, v19, v23
	v_cvt_pk_bf16_f32 v201, v27, v31
	v_cvt_pk_bf16_f32 v202, v4, v8
	v_cvt_pk_bf16_f32 v203, v12, v16
	v_cvt_pk_bf16_f32 v204, v20, v24
	v_cvt_pk_bf16_f32 v205, v28, v32
	v_cvt_pk_bf16_f32 v206, v5, v9
	v_cvt_pk_bf16_f32 v207, v13, v17
	v_cvt_pk_bf16_f32 v208, v21, v25
	v_cvt_pk_bf16_f32 v209, v29, v33
	v_xor_b32_e32 v211, 64, v210
	v_xor_b32_e32 v212, 0x80, v210
	v_xor_b32_e32 v213, 0xc0, v210
	s_lshl_b32 s10, s50, 16
	s_lshl_b64 s[28:29], s[10:11], 2
	s_add_u32 s28, s47, s28
	s_addc_u32 s29, s21, s29
	s_add_u32 s30, s28, 0x1000
	global_load_dwordx4 v[2:5], v240, s[28:29] offset:0
	s_addc_u32 s31, s29, 0
	global_load_dwordx4 v[6:9], v240, s[30:31] offset:0
	s_add_u32 s30, s28, 0x2000
	s_addc_u32 s31, s29, 0
	global_load_dwordx4 v[10:13], v240, s[30:31] offset:0
	s_add_u32 s30, s28, 0x3000
	s_addc_u32 s31, s29, 0
	global_load_dwordx4 v[14:17], v240, s[30:31] offset:0
	s_add_u32 s30, s28, 0x4000
	s_addc_u32 s31, s29, 0
	global_load_dwordx4 v[18:21], v240, s[30:31] offset:0
	s_add_u32 s30, s28, 0x5000
	s_addc_u32 s31, s29, 0
	global_load_dwordx4 v[22:25], v240, s[30:31] offset:0
	s_add_u32 s30, s28, 0x6000
	s_addc_u32 s31, s29, 0
	global_load_dwordx4 v[26:29], v240, s[30:31] offset:0
	s_add_u32 s28, s28, 0x7000
	s_mov_b32 m0, s39
	s_addc_u32 s29, s29, 0
	global_load_dwordx4 v[30:33], v240, s[28:29] offset:0
	ds_write_b128 v210, v[194:197]
	ds_write_b128 v211, v[198:201]
	ds_write_b128 v212, v[202:205]
	ds_write_b128 v213, v[206:209]
	ds_read_b128 v[218:221], v248 offset:49152
	ds_read_b128 v[222:225], v248 offset:50176
	ds_read_b128 v[210:213], v248 offset:51200
	ds_read_b128 v[214:217], v248 offset:52224
	ds_read_b128 v[202:205], v248 offset:53248
	ds_read_b128 v[206:209], v248 offset:54272
	ds_read_b128 v[194:197], v248 offset:55296
	ds_read_b128 v[198:201], v248 offset:56320
	v_lshl_add_u64 v[238:239], v[238:239], 0, s[16:17]
	global_load_lds_dwordx4 v[238:239], off
	v_lshl_add_u64 v[236:237], v[236:237], 0, s[16:17]
	s_mov_b32 m0, s40
	s_and_b64 vcc, exec, s[4:5]
	global_load_lds_dwordx4 v[236:237], off
	s_waitcnt vmcnt(12)
	s_waitcnt lgkmcnt(0)
	s_barrier
	s_cbranch_vccnz .LBB0_2447
	s_setprio 1
	s_waitcnt lgkmcnt(0)
	v_mfma_f32_16x16x32_bf16 v[94:97], v[178:181], v[218:221], v[94:97]
	v_mfma_f32_16x16x32_bf16 v[90:93], v[186:189], v[218:221], v[90:93]
	v_mfma_f32_16x16x32_bf16 v[78:81], v[178:181], v[210:213], v[78:81]
	v_mfma_f32_16x16x32_bf16 v[74:77], v[186:189], v[210:213], v[74:77]
	v_mfma_f32_16x16x32_bf16 v[62:65], v[178:181], v[202:205], v[62:65]
	v_mfma_f32_16x16x32_bf16 v[58:61], v[186:189], v[202:205], v[58:61]
	v_mfma_f32_16x16x32_bf16 v[46:49], v[178:181], v[194:197], v[46:49]
	v_mfma_f32_16x16x32_bf16 v[42:45], v[186:189], v[194:197], v[42:45]
	v_mfma_f32_16x16x32_bf16 v[94:97], v[182:185], v[222:225], v[94:97]
	v_mfma_f32_16x16x32_bf16 v[90:93], v[190:193], v[222:225], v[90:93]
	v_mfma_f32_16x16x32_bf16 v[78:81], v[182:185], v[214:217], v[78:81]
	v_mfma_f32_16x16x32_bf16 v[74:77], v[190:193], v[214:217], v[74:77]
	v_mfma_f32_16x16x32_bf16 v[62:65], v[182:185], v[206:209], v[62:65]
	v_mfma_f32_16x16x32_bf16 v[58:61], v[190:193], v[206:209], v[58:61]
	v_mfma_f32_16x16x32_bf16 v[46:49], v[182:185], v[198:201], v[46:49]
	v_mfma_f32_16x16x32_bf16 v[42:45], v[190:193], v[198:201], v[42:45]
	s_setprio 0
	s_setprio 1
	v_mfma_f32_16x16x32_bf16 v[86:89], v[162:165], v[218:221], v[86:89]
	v_mfma_f32_16x16x32_bf16 v[82:85], v[170:173], v[218:221], v[82:85]
	v_mfma_f32_16x16x32_bf16 v[70:73], v[162:165], v[210:213], v[70:73]
	v_mfma_f32_16x16x32_bf16 v[66:69], v[170:173], v[210:213], v[66:69]
	v_mfma_f32_16x16x32_bf16 v[54:57], v[162:165], v[202:205], v[54:57]
	v_mfma_f32_16x16x32_bf16 v[50:53], v[170:173], v[202:205], v[50:53]
	v_mfma_f32_16x16x32_bf16 v[38:41], v[162:165], v[194:197], v[38:41]
	v_mfma_f32_16x16x32_bf16 v[34:37], v[170:173], v[194:197], v[34:37]
	v_mfma_f32_16x16x32_bf16 v[86:89], v[166:169], v[222:225], v[86:89]
	v_mfma_f32_16x16x32_bf16 v[82:85], v[174:177], v[222:225], v[82:85]
	v_mfma_f32_16x16x32_bf16 v[70:73], v[166:169], v[214:217], v[70:73]
	v_mfma_f32_16x16x32_bf16 v[66:69], v[174:177], v[214:217], v[66:69]
	v_mfma_f32_16x16x32_bf16 v[54:57], v[166:169], v[206:209], v[54:57]
	v_mfma_f32_16x16x32_bf16 v[50:53], v[174:177], v[206:209], v[50:53]
	v_mfma_f32_16x16x32_bf16 v[38:41], v[166:169], v[198:201], v[38:41]
	v_mfma_f32_16x16x32_bf16 v[34:37], v[174:177], v[198:201], v[34:37]
	s_setprio 0
	s_branch .LBB0_2447

; #define PG8_BWAIT(n) asm volatile("s_waitcnt vmcnt(" #n ")" : "+v"(bv[0]), "+v"(bv[1]), "+v"(bv[2]), "+v"(bv[3]), "+v"(bv[4]), "+v"(bv[5]), "+v"(bv[6]), "+v"(bv[7]) :: "memory")
; #define PG8_STAGE_A(bufoff, V0, V1, kb) do { \
;         __builtin_amdgcn_global_load_lds((const unsigned*)((Abase + (kb)) + (V0)), (LAS unsigned*)(lds + (bufoff) + ldsw), 16, 0, 0); \
;         __builtin_amdgcn_global_load_lds((const unsigned*)((Abase + (kb)) + (V1)), (LAS unsigned*)(lds + (bufoff) + ldsw + 8192), 16, 0, 0); } while (0)
; #define PG8_LDA(dst, b, h) do { _Pragma("unroll") for (int m = 0; m < 4; ++m) _Pragma("unroll") for (int k = 0; k < 2; ++k) dst[m][k] = *(const LAS bf16x8*)(lds + PG8_SA(b, h) + aoff + m * 2048 + k * 1024); } while (0)
; #define PG8_LDB(dst, b, h) do { _Pragma("unroll") for (int n = 0; n < 2; ++n) _Pragma("unroll") for (int k = 0; k < 2; ++k) dst[n][k] = *(const LAS bf16x8*)(lds + PG8_SB(b, h) + boff + n * 2048 + k * 1024); } while (0)
; #define PG8_MMA(ai, bj, At, Bt) do { __builtin_amdgcn_s_setprio(1); _Pragma("unroll") for (int m = 0; m < 4; ++m) _Pragma("unroll") for (int n = 0; n < 2; ++n) _Pragma("unroll") for (int k = 0; k < 2; ++k) \
;         acc[ai][bj][m][n] = __builtin_amdgcn_mfma_f32_16x16x32_bf16(Bt[n][k], At[m][k], acc[ai][bj][m][n], 0, 0, 0); __builtin_amdgcn_s_setprio(0); } while (0)
; #define PG8_WAIT_V(n) asm volatile("s_waitcnt vmcnt(" #n ")" ::: "memory")
; #define PG8_WAIT_L(n) asm volatile("s_waitcnt lgkmcnt(" #n ")" ::: "memory")
; #define PG8_BAR __builtin_amdgcn_s_barrier()
; #define PG8_SCHED __builtin_amdgcn_sched_barrier(0)
; template <class Epi, class Sched, bool ALIGN_EPI>
; __device__ __forceinline__ void gemm_phase(LAS unsigned char* lds, const Gemm g, const Sched& S, const Epi& E) {
;     ...
;             PG8_LDB(B0, 0, 0); PG8_LDB(B1, 0, 1); PG8_SCHED; PG8_LDA(At, 0, 0); PG8_STAGE_A(PG8_SA(1, 1), vc10, vc11, kb1);
;             PG8_WAIT_V(12); PG8_WAIT_L(0); PG8_BAR; PG8_MMA(0, 0, At, B0); PG8_MMA(0, 1, At, B1); PG8_BAR; PG8_SCHED;
;             if (last) { vc10 = vn10; vc11 = vn11; }
;             PG8_BWAIT(2); PG8_BCOMMIT(0); PG8_SCHED; PG8_LDA(At, 0, 1); PG8_BISSUE(t + 3 >= nt ? pbn + (size_t)(t + 3 - nt) * 64 * Sched::LDN : pbc + (size_t)(t + 3) * 64 * Sched::LDN); PG8_STAGE_A(PG8_SA(0, 0), vc00, vc01, kb2);
.LBB0_4711:
	s_add_i32 s54, s53, 2
	s_add_i32 m0, s40, 0xc000
	s_add_u32 s2, s90, s22
	s_addc_u32 s3, s91, s23
	global_load_lds_dwordx4 v233, s[2:3]
	s_add_i32 m0, s40, 0xe000
	s_nop 0
	global_load_lds_dwordx4 v234, s[2:3]
	v_add_u32_e32 v162, 0x10000, v240
	v_add_u32_e32 v174, 0x14000, v240
	ds_read_b128 v[178:181], v162
	ds_read_b128 v[182:185], v162 offset:1024
	ds_read_b128 v[186:189], v162 offset:2048
	ds_read_b128 v[190:193], v162 offset:3072
	ds_read_b128 v[162:165], v174
	ds_read_b128 v[166:169], v174 offset:1024
	ds_read_b128 v[170:173], v174 offset:2048
	ds_read_b128 v[174:177], v174 offset:3072
	s_waitcnt lgkmcnt(0)
	ds_read_b128 v[194:197], v241
	ds_read_b128 v[198:201], v241 offset:1024
	ds_read_b128 v[202:205], v241 offset:2048
	ds_read_b128 v[206:209], v241 offset:3072
	ds_read_b128 v[210:213], v241 offset:4096
	ds_read_b128 v[214:217], v241 offset:5120
	ds_read_b128 v[218:221], v241 offset:6144
	ds_read_b128 v[222:225], v241 offset:7168
	s_waitcnt vmcnt(12)
	s_waitcnt lgkmcnt(0)
	s_barrier
	s_setprio 1
	s_waitcnt lgkmcnt(0)
	v_mfma_f32_16x16x32_bf16 v[158:161], v[178:181], v[194:197], v[158:161]
	v_mfma_f32_16x16x32_bf16 v[154:157], v[186:189], v[194:197], v[154:157]
	v_mfma_f32_16x16x32_bf16 v[142:145], v[178:181], v[202:205], v[142:145]
	v_mfma_f32_16x16x32_bf16 v[138:141], v[186:189], v[202:205], v[138:141]
	v_mfma_f32_16x16x32_bf16 v[126:129], v[178:181], v[210:213], v[126:129]
	v_mfma_f32_16x16x32_bf16 v[122:125], v[186:189], v[210:213], v[122:125]
	v_mfma_f32_16x16x32_bf16 v[110:113], v[178:181], v[218:221], v[110:113]
	v_mfma_f32_16x16x32_bf16 v[106:109], v[186:189], v[218:221], v[106:109]
	v_mfma_f32_16x16x32_bf16 v[158:161], v[182:185], v[198:201], v[158:161]
	v_mfma_f32_16x16x32_bf16 v[154:157], v[190:193], v[198:201], v[154:157]
	v_mfma_f32_16x16x32_bf16 v[142:145], v[182:185], v[206:209], v[142:145]
	v_mfma_f32_16x16x32_bf16 v[138:141], v[190:193], v[206:209], v[138:141]
	v_mfma_f32_16x16x32_bf16 v[126:129], v[182:185], v[214:217], v[126:129]
	v_mfma_f32_16x16x32_bf16 v[122:125], v[190:193], v[214:217], v[122:125]
	v_mfma_f32_16x16x32_bf16 v[110:113], v[182:185], v[222:225], v[110:113]
	v_mfma_f32_16x16x32_bf16 v[106:109], v[190:193], v[222:225], v[106:109]
	s_setprio 0
	s_setprio 1
	v_mfma_f32_16x16x32_bf16 v[150:153], v[162:165], v[194:197], v[150:153]
	v_mfma_f32_16x16x32_bf16 v[146:149], v[170:173], v[194:197], v[146:149]
	v_mfma_f32_16x16x32_bf16 v[134:137], v[162:165], v[202:205], v[134:137]
	v_mfma_f32_16x16x32_bf16 v[130:133], v[170:173], v[202:205], v[130:133]
	v_mfma_f32_16x16x32_bf16 v[118:121], v[162:165], v[210:213], v[118:121]
	v_mfma_f32_16x16x32_bf16 v[114:117], v[170:173], v[210:213], v[114:117]
	v_mfma_f32_16x16x32_bf16 v[102:105], v[162:165], v[218:221], v[102:105]
	v_mfma_f32_16x16x32_bf16 v[98:101], v[170:173], v[218:221], v[98:101]
	v_mfma_f32_16x16x32_bf16 v[150:153], v[166:169], v[198:201], v[150:153]
	v_mfma_f32_16x16x32_bf16 v[146:149], v[174:177], v[198:201], v[146:149]
	v_mfma_f32_16x16x32_bf16 v[134:137], v[166:169], v[206:209], v[134:137]
	v_mfma_f32_16x16x32_bf16 v[130:133], v[174:177], v[206:209], v[130:133]
	v_mfma_f32_16x16x32_bf16 v[118:121], v[166:169], v[214:217], v[118:121]
	v_mfma_f32_16x16x32_bf16 v[114:117], v[174:177], v[214:217], v[114:117]
	v_mfma_f32_16x16x32_bf16 v[102:105], v[166:169], v[222:225], v[102:105]
	v_mfma_f32_16x16x32_bf16 v[98:101], v[174:177], v[222:225], v[98:101]
	s_setprio 0
	s_barrier
	s_waitcnt vmcnt(2)
	s_nop 0
	v_add_u32_e32 v210, 0x10000, v235
	v_cvt_pk_bf16_f32 v194, v2, v6
	v_cvt_pk_bf16_f32 v195, v10, v14
	v_cvt_pk_bf16_f32 v196, v18, v22
	v_cvt_pk_bf16_f32 v197, v26, v30
	v_cvt_pk_bf16_f32 v198, v3, v7
	v_cvt_pk_bf16_f32 v199, v11, v15
	v_cvt_pk_bf16_f32 v200, v19, v23
	v_cvt_pk_bf16_f32 v201, v27, v31
	v_cvt_pk_bf16_f32 v202, v4, v8
	v_cvt_pk_bf16_f32 v203, v12, v16
	v_cvt_pk_bf16_f32 v204, v20, v24
	v_cvt_pk_bf16_f32 v205, v28, v32
	v_cvt_pk_bf16_f32 v206, v5, v9
	v_cvt_pk_bf16_f32 v207, v13, v17
	v_cvt_pk_bf16_f32 v208, v21, v25
	v_cvt_pk_bf16_f32 v209, v29, v33
	v_xor_b32_e32 v211, 64, v210
	v_xor_b32_e32 v212, 0x80, v210
	v_xor_b32_e32 v213, 0xc0, v210
	s_cmp_lt_u32 s54, 13
	s_mov_b64 s[4:5], -1
	s_cbranch_scc0 .LBB0_4713
	s_add_u32 s2, s20, 0x30000
	s_addc_u32 s3, s21, 0
	s_mov_b64 s[4:5], 0

; #define PG8_BWAIT(n) asm volatile("s_waitcnt vmcnt(" #n ")" : "+v"(bv[0]), "+v"(bv[1]), "+v"(bv[2]), "+v"(bv[3]), "+v"(bv[4]), "+v"(bv[5]), "+v"(bv[6]), "+v"(bv[7]) :: "memory")
; #define PG8_STAGE_A(bufoff, V0, V1, kb) do { \
;         __builtin_amdgcn_global_load_lds((const unsigned*)((Abase + (kb)) + (V0)), (LAS unsigned*)(lds + (bufoff) + ldsw), 16, 0, 0); \
;         __builtin_amdgcn_global_load_lds((const unsigned*)((Abase + (kb)) + (V1)), (LAS unsigned*)(lds + (bufoff) + ldsw + 8192), 16, 0, 0); } while (0)
; #define PG8_LDA(dst, b, h) do { _Pragma("unroll") for (int m = 0; m < 4; ++m) _Pragma("unroll") for (int k = 0; k < 2; ++k) dst[m][k] = *(const LAS bf16x8*)(lds + PG8_SA(b, h) + aoff + m * 2048 + k * 1024); } while (0)
; #define PG8_LDB(dst, b, h) do { _Pragma("unroll") for (int n = 0; n < 2; ++n) _Pragma("unroll") for (int k = 0; k < 2; ++k) dst[n][k] = *(const LAS bf16x8*)(lds + PG8_SB(b, h) + boff + n * 2048 + k * 1024); } while (0)
; #define PG8_MMA(ai, bj, At, Bt) do { __builtin_amdgcn_s_setprio(1); _Pragma("unroll") for (int m = 0; m < 4; ++m) _Pragma("unroll") for (int n = 0; n < 2; ++n) _Pragma("unroll") for (int k = 0; k < 2; ++k) \
;         acc[ai][bj][m][n] = __builtin_amdgcn_mfma_f32_16x16x32_bf16(Bt[n][k], At[m][k], acc[ai][bj][m][n], 0, 0, 0); __builtin_amdgcn_s_setprio(0); } while (0)
; #define PG8_WAIT_V(n) asm volatile("s_waitcnt vmcnt(" #n ")" ::: "memory")
; #define PG8_WAIT_L(n) asm volatile("s_waitcnt lgkmcnt(" #n ")" ::: "memory")
; #define PG8_BAR __builtin_amdgcn_s_barrier()
; #define PG8_SCHED __builtin_amdgcn_sched_barrier(0)
; template <class Epi, class Sched, bool ALIGN_EPI>
; __device__ __forceinline__ void gemm_phase(LAS unsigned char* lds, const Gemm g, const Sched& S, const Epi& E) {
;     ...
;             PG8_LDB(B0, 1, 0); PG8_LDB(B1, 1, 1); PG8_SCHED; PG8_LDA(At, 1, 0); PG8_STAGE_A(PG8_SA(0, 1), vc10, vc11, kb2);
;             PG8_WAIT_V(12); PG8_WAIT_L(0); PG8_BAR; PG8_MMA(0, 0, At, B0); PG8_MMA(0, 1, At, B1); PG8_BAR; PG8_SCHED;
;             PG8_BWAIT(2); PG8_BCOMMIT(1); PG8_SCHED; PG8_LDA(At, 1, 1); PG8_BISSUE(t + 4 >= nt ? pbn + (size_t)(t + 4 - nt) * 64 * Sched::LDN : pbc + (size_t)(t + 4) * 64 * Sched::LDN); PG8_STAGE_A(PG8_SA(1, 0), vc00, vc01, kb2 + 128u);
.LBB0_4717:
	v_cndmask_b32_e64 v234, v234, v245, s[4:5]
	v_cndmask_b32_e64 v233, v233, v244, s[4:5]
	s_barrier
	s_mov_b32 m0, s42
	s_nop 0
	global_load_lds_dwordx4 v233, s[26:27]
	s_mov_b32 m0, s43
	s_nop 0
	global_load_lds_dwordx4 v234, s[26:27]
	v_add_u32_e32 v162, 0x18000, v240
	v_add_u32_e32 v174, 0x1c000, v240
	ds_read_b128 v[178:181], v162
	ds_read_b128 v[182:185], v162 offset:1024
	ds_read_b128 v[186:189], v162 offset:2048
	ds_read_b128 v[190:193], v162 offset:3072
	ds_read_b128 v[162:165], v174
	ds_read_b128 v[166:169], v174 offset:1024
	ds_read_b128 v[170:173], v174 offset:2048
	ds_read_b128 v[174:177], v174 offset:3072
	s_waitcnt lgkmcnt(0)
	ds_read_b128 v[194:197], v241 offset:32768
	ds_read_b128 v[198:201], v241 offset:33792
	ds_read_b128 v[202:205], v241 offset:34816
	ds_read_b128 v[206:209], v241 offset:35840
	ds_read_b128 v[210:213], v241 offset:36864
	ds_read_b128 v[214:217], v241 offset:37888
	ds_read_b128 v[218:221], v241 offset:38912
	ds_read_b128 v[222:225], v241 offset:39936
	s_waitcnt vmcnt(12)
	s_waitcnt lgkmcnt(0)
	s_barrier
	s_setprio 1
	s_waitcnt lgkmcnt(0)
	v_mfma_f32_16x16x32_bf16 v[158:161], v[178:181], v[194:197], v[158:161]
	v_mfma_f32_16x16x32_bf16 v[154:157], v[186:189], v[194:197], v[154:157]
	v_mfma_f32_16x16x32_bf16 v[142:145], v[178:181], v[202:205], v[142:145]
	v_mfma_f32_16x16x32_bf16 v[138:141], v[186:189], v[202:205], v[138:141]
	v_mfma_f32_16x16x32_bf16 v[126:129], v[178:181], v[210:213], v[126:129]
	v_mfma_f32_16x16x32_bf16 v[122:125], v[186:189], v[210:213], v[122:125]
	v_mfma_f32_16x16x32_bf16 v[110:113], v[178:181], v[218:221], v[110:113]
	v_mfma_f32_16x16x32_bf16 v[106:109], v[186:189], v[218:221], v[106:109]
	v_mfma_f32_16x16x32_bf16 v[158:161], v[182:185], v[198:201], v[158:161]
	v_mfma_f32_16x16x32_bf16 v[154:157], v[190:193], v[198:201], v[154:157]
	v_mfma_f32_16x16x32_bf16 v[142:145], v[182:185], v[206:209], v[142:145]
	v_mfma_f32_16x16x32_bf16 v[138:141], v[190:193], v[206:209], v[138:141]
	v_mfma_f32_16x16x32_bf16 v[126:129], v[182:185], v[214:217], v[126:129]
	v_mfma_f32_16x16x32_bf16 v[122:125], v[190:193], v[214:217], v[122:125]
	v_mfma_f32_16x16x32_bf16 v[110:113], v[182:185], v[222:225], v[110:113]
	v_mfma_f32_16x16x32_bf16 v[106:109], v[190:193], v[222:225], v[106:109]
	s_setprio 0
	s_setprio 1
	v_mfma_f32_16x16x32_bf16 v[150:153], v[162:165], v[194:197], v[150:153]
	v_mfma_f32_16x16x32_bf16 v[146:149], v[170:173], v[194:197], v[146:149]
	v_mfma_f32_16x16x32_bf16 v[134:137], v[162:165], v[202:205], v[134:137]
	v_mfma_f32_16x16x32_bf16 v[130:133], v[170:173], v[202:205], v[130:133]
	v_mfma_f32_16x16x32_bf16 v[118:121], v[162:165], v[210:213], v[118:121]
	v_mfma_f32_16x16x32_bf16 v[114:117], v[170:173], v[210:213], v[114:117]
	v_mfma_f32_16x16x32_bf16 v[102:105], v[162:165], v[218:221], v[102:105]
	v_mfma_f32_16x16x32_bf16 v[98:101], v[170:173], v[218:221], v[98:101]
	v_mfma_f32_16x16x32_bf16 v[150:153], v[166:169], v[198:201], v[150:153]
	v_mfma_f32_16x16x32_bf16 v[146:149], v[174:177], v[198:201], v[146:149]
	v_mfma_f32_16x16x32_bf16 v[134:137], v[166:169], v[206:209], v[134:137]
	v_mfma_f32_16x16x32_bf16 v[130:133], v[174:177], v[206:209], v[130:133]
	v_mfma_f32_16x16x32_bf16 v[118:121], v[166:169], v[214:217], v[118:121]
	v_mfma_f32_16x16x32_bf16 v[114:117], v[174:177], v[214:217], v[114:117]
	v_mfma_f32_16x16x32_bf16 v[102:105], v[166:169], v[222:225], v[102:105]
	v_mfma_f32_16x16x32_bf16 v[98:101], v[174:177], v[222:225], v[98:101]
	s_setprio 0
	s_barrier
	s_waitcnt vmcnt(2)
	s_nop 0
	v_add_u32_e32 v210, 0x18000, v235
	v_cvt_pk_bf16_f32 v194, v2, v6
	v_cvt_pk_bf16_f32 v195, v10, v14
	v_cvt_pk_bf16_f32 v196, v18, v22
	v_cvt_pk_bf16_f32 v197, v26, v30
	v_cvt_pk_bf16_f32 v198, v3, v7
	v_cvt_pk_bf16_f32 v199, v11, v15
	v_cvt_pk_bf16_f32 v200, v19, v23
	v_cvt_pk_bf16_f32 v201, v27, v31
	v_cvt_pk_bf16_f32 v202, v4, v8
	v_cvt_pk_bf16_f32 v203, v12, v16
	v_cvt_pk_bf16_f32 v204, v20, v24
	v_cvt_pk_bf16_f32 v205, v28, v32
	v_cvt_pk_bf16_f32 v206, v5, v9
	v_cvt_pk_bf16_f32 v207, v13, v17
	v_cvt_pk_bf16_f32 v208, v21, v25
	v_cvt_pk_bf16_f32 v209, v29, v33
	v_xor_b32_e32 v211, 64, v210
	v_xor_b32_e32 v212, 0x80, v210
	v_xor_b32_e32 v213, 0xc0, v210
	s_cmp_lt_u32 s54, 12
	s_mov_b64 s[28:29], -1
	s_cbranch_scc0 .LBB0_4719
	s_add_u32 s4, s20, 0x40000
	s_addc_u32 s5, s21, 0
	s_mov_b64 s[28:29], 0

; #define PG8_BWAIT(n) asm volatile("s_waitcnt vmcnt(" #n ")" : "+v"(bv[0]), "+v"(bv[1]), "+v"(bv[2]), "+v"(bv[3]), "+v"(bv[4]), "+v"(bv[5]), "+v"(bv[6]), "+v"(bv[7]) :: "memory")
; #define PG8_STAGE_A(bufoff, V0, V1, kb) do { \
;         __builtin_amdgcn_global_load_lds((const unsigned*)((Abase + (kb)) + (V0)), (LAS unsigned*)(lds + (bufoff) + ldsw), 16, 0, 0); \
;         __builtin_amdgcn_global_load_lds((const unsigned*)((Abase + (kb)) + (V1)), (LAS unsigned*)(lds + (bufoff) + ldsw + 8192), 16, 0, 0); } while (0)
; #define PG8_LDA(dst, b, h) do { _Pragma("unroll") for (int m = 0; m < 4; ++m) _Pragma("unroll") for (int k = 0; k < 2; ++k) dst[m][k] = *(const LAS bf16x8*)(lds + PG8_SA(b, h) + aoff + m * 2048 + k * 1024); } while (0)
; #define PG8_LDB(dst, b, h) do { _Pragma("unroll") for (int n = 0; n < 2; ++n) _Pragma("unroll") for (int k = 0; k < 2; ++k) dst[n][k] = *(const LAS bf16x8*)(lds + PG8_SB(b, h) + boff + n * 2048 + k * 1024); } while (0)
; #define PG8_MMA(ai, bj, At, Bt) do { __builtin_amdgcn_s_setprio(1); _Pragma("unroll") for (int m = 0; m < 4; ++m) _Pragma("unroll") for (int n = 0; n < 2; ++n) _Pragma("unroll") for (int k = 0; k < 2; ++k) \
;         acc[ai][bj][m][n] = __builtin_amdgcn_mfma_f32_16x16x32_bf16(Bt[n][k], At[m][k], acc[ai][bj][m][n], 0, 0, 0); __builtin_amdgcn_s_setprio(0); } while (0)
; #define PG8_WAIT_V(n) asm volatile("s_waitcnt vmcnt(" #n ")" ::: "memory")
; #define PG8_WAIT_L(n) asm volatile("s_waitcnt lgkmcnt(" #n ")" ::: "memory")
; #define PG8_BAR __builtin_amdgcn_s_barrier()
; template <class Epi, class Sched, bool ALIGN_EPI>
; __device__ __forceinline__ void gemm_phase(LAS unsigned char* lds, const Gemm g, const Sched& S, const Epi& E) {
;     ...
;             PG8_LDB(B0, 0, 0); PG8_LDB(B1, 0, 1); PG8_SCHED; PG8_LDA(At, 0, 0); PG8_STAGE_A(PG8_SA(1, 1), vc10, vc11, kb1);
;             PG8_WAIT_V(12); PG8_WAIT_L(0); PG8_BAR; PG8_MMA(0, 0, At, B0); PG8_MMA(0, 1, At, B1); PG8_BAR; PG8_SCHED;
;             if (last) { vc10 = vn10; vc11 = vn11; }
;             PG8_BWAIT(2); PG8_BCOMMIT(0); PG8_SCHED; PG8_LDA(At, 0, 1); PG8_BISSUE(t + 3 >= nt ? pbn + (size_t)(t + 3 - nt) * 64 * Sched::LDN : pbc + (size_t)(t + 3) * 64 * Sched::LDN); PG8_STAGE_A(PG8_SA(0, 0), vc00, vc01, kb2);
;             PG8_WAIT_V(12); PG8_WAIT_L(0); PG8_BAR; if (half1) { PG8_MMA(1, 0, At, B0); PG8_MMA(1, 1, At, B1); } PG8_BAR; PG8_SCHED;
.LBB0_4908:
	s_lshl_b32 s3, s52, 7
	s_add_i32 s2, s3, 0x100
	v_cndmask_b32_e64 v228, v228, v250, s[28:29]
	v_readlane_b32 s56, v254, 53
	v_readlane_b32 s57, v254, 54
	s_add_u32 s30, s56, s3
	s_addc_u32 s31, s57, 0
	v_lshl_add_u64 v[236:237], s[30:31], 0, v[230:231]
	v_lshl_add_u64 v[236:237], v[236:237], 0, s[14:15]
	s_add_i32 m0, s37, 0xc000
	v_mov_b32_e32 v233, v231
	global_load_lds_dwordx4 v[236:237], off
	v_lshl_add_u64 v[236:237], s[30:31], 0, v[232:233]
	v_lshl_add_u64 v[236:237], v[236:237], 0, s[14:15]
	s_add_i32 m0, s37, 0xe000
	s_nop 0
	global_load_lds_dwordx4 v[236:237], off
	v_add_u32_e32 v162, 0x10000, v247
	v_add_u32_e32 v174, 0x14000, v247
	ds_read_b128 v[178:181], v162
	ds_read_b128 v[182:185], v162 offset:1024
	ds_read_b128 v[186:189], v162 offset:2048
	ds_read_b128 v[190:193], v162 offset:3072
	ds_read_b128 v[162:165], v174
	ds_read_b128 v[166:169], v174 offset:1024
	ds_read_b128 v[170:173], v174 offset:2048
	ds_read_b128 v[174:177], v174 offset:3072
	s_waitcnt lgkmcnt(0)
	ds_read_b128 v[194:197], v248
	ds_read_b128 v[198:201], v248 offset:1024
	ds_read_b128 v[202:205], v248 offset:2048
	ds_read_b128 v[206:209], v248 offset:3072
	ds_read_b128 v[210:213], v248 offset:4096
	ds_read_b128 v[214:217], v248 offset:5120
	ds_read_b128 v[218:221], v248 offset:6144
	ds_read_b128 v[222:225], v248 offset:7168
	s_waitcnt vmcnt(12)
	s_waitcnt lgkmcnt(0)
	s_barrier
	s_setprio 1
	s_waitcnt lgkmcnt(0)
	v_mfma_f32_16x16x32_bf16 v[158:161], v[178:181], v[194:197], v[158:161]
	v_mfma_f32_16x16x32_bf16 v[154:157], v[186:189], v[194:197], v[154:157]
	v_mfma_f32_16x16x32_bf16 v[142:145], v[178:181], v[202:205], v[142:145]
	v_mfma_f32_16x16x32_bf16 v[138:141], v[186:189], v[202:205], v[138:141]
	v_mfma_f32_16x16x32_bf16 v[126:129], v[178:181], v[210:213], v[126:129]
	v_mfma_f32_16x16x32_bf16 v[122:125], v[186:189], v[210:213], v[122:125]
	v_mfma_f32_16x16x32_bf16 v[110:113], v[178:181], v[218:221], v[110:113]
	v_mfma_f32_16x16x32_bf16 v[106:109], v[186:189], v[218:221], v[106:109]
	v_mfma_f32_16x16x32_bf16 v[158:161], v[182:185], v[198:201], v[158:161]
	v_mfma_f32_16x16x32_bf16 v[154:157], v[190:193], v[198:201], v[154:157]
	v_mfma_f32_16x16x32_bf16 v[142:145], v[182:185], v[206:209], v[142:145]
	v_mfma_f32_16x16x32_bf16 v[138:141], v[190:193], v[206:209], v[138:141]
	v_mfma_f32_16x16x32_bf16 v[126:129], v[182:185], v[214:217], v[126:129]
	v_mfma_f32_16x16x32_bf16 v[122:125], v[190:193], v[214:217], v[122:125]
	v_mfma_f32_16x16x32_bf16 v[110:113], v[182:185], v[222:225], v[110:113]
	v_mfma_f32_16x16x32_bf16 v[106:109], v[190:193], v[222:225], v[106:109]
	s_setprio 0
	s_setprio 1
	v_mfma_f32_16x16x32_bf16 v[150:153], v[162:165], v[194:197], v[150:153]
	v_mfma_f32_16x16x32_bf16 v[146:149], v[170:173], v[194:197], v[146:149]
	v_mfma_f32_16x16x32_bf16 v[134:137], v[162:165], v[202:205], v[134:137]
	v_mfma_f32_16x16x32_bf16 v[130:133], v[170:173], v[202:205], v[130:133]
	v_mfma_f32_16x16x32_bf16 v[118:121], v[162:165], v[210:213], v[118:121]
	v_mfma_f32_16x16x32_bf16 v[114:117], v[170:173], v[210:213], v[114:117]
	v_mfma_f32_16x16x32_bf16 v[102:105], v[162:165], v[218:221], v[102:105]
	v_mfma_f32_16x16x32_bf16 v[98:101], v[170:173], v[218:221], v[98:101]
	v_mfma_f32_16x16x32_bf16 v[150:153], v[166:169], v[198:201], v[150:153]
	v_mfma_f32_16x16x32_bf16 v[146:149], v[174:177], v[198:201], v[146:149]
	v_mfma_f32_16x16x32_bf16 v[134:137], v[166:169], v[206:209], v[134:137]
	v_mfma_f32_16x16x32_bf16 v[130:133], v[174:177], v[206:209], v[130:133]
	v_mfma_f32_16x16x32_bf16 v[118:121], v[166:169], v[214:217], v[118:121]
	v_mfma_f32_16x16x32_bf16 v[114:117], v[174:177], v[214:217], v[114:117]
	v_mfma_f32_16x16x32_bf16 v[102:105], v[166:169], v[222:225], v[102:105]
	v_mfma_f32_16x16x32_bf16 v[98:101], v[174:177], v[222:225], v[98:101]
	s_setprio 0
	s_barrier
	s_waitcnt vmcnt(2)
	v_cndmask_b32_e64 v226, v226, v249, s[28:29]
	v_add_u32_e32 v210, 0x10000, v242
	v_cvt_pk_bf16_f32 v194, v2, v6
	v_cvt_pk_bf16_f32 v195, v10, v14
	v_cvt_pk_bf16_f32 v196, v18, v22
	v_cvt_pk_bf16_f32 v197, v26, v30
	v_cvt_pk_bf16_f32 v198, v3, v7
	v_cvt_pk_bf16_f32 v199, v11, v15
	v_cvt_pk_bf16_f32 v200, v19, v23
	v_cvt_pk_bf16_f32 v201, v27, v31
	v_cvt_pk_bf16_f32 v202, v4, v8
	v_cvt_pk_bf16_f32 v203, v12, v16
	v_cvt_pk_bf16_f32 v204, v20, v24
	v_cvt_pk_bf16_f32 v205, v28, v32
	v_cvt_pk_bf16_f32 v206, v5, v9
	v_cvt_pk_bf16_f32 v207, v13, v17
	v_cvt_pk_bf16_f32 v208, v21, v25
	v_cvt_pk_bf16_f32 v209, v29, v33
	v_xor_b32_e32 v211, 64, v210
	v_xor_b32_e32 v212, 0x80, v210
	v_xor_b32_e32 v213, 0xc0, v210
	s_add_i32 s8, s52, -1
	s_lshl_b64 s[30:31], s[8:9], 18
	s_add_u32 s3, s49, s30
	s_addc_u32 s8, s21, s31
	s_and_b64 s[30:31], s[26:27], exec
	s_cselect_b32 s30, s50, s3
	s_cselect_b32 s31, s51, s8
	s_add_u32 s54, s30, 0x1000
	global_load_dwordx4 v[2:5], v240, s[30:31] offset:0
	s_addc_u32 s55, s31, 0
	global_load_dwordx4 v[6:9], v240, s[54:55] offset:0
	s_add_u32 s54, s30, 0x2000
	s_addc_u32 s55, s31, 0
	global_load_dwordx4 v[10:13], v240, s[54:55] offset:0
	s_add_u32 s54, s30, 0x3000
	s_addc_u32 s55, s31, 0
	global_load_dwordx4 v[14:17], v240, s[54:55] offset:0
	s_add_u32 s54, s30, 0x4000
	s_addc_u32 s55, s31, 0
	global_load_dwordx4 v[18:21], v240, s[54:55] offset:0
	s_add_u32 s54, s30, 0x5000
	s_addc_u32 s55, s31, 0
	global_load_dwordx4 v[22:25], v240, s[54:55] offset:0
	s_add_u32 s54, s30, 0x6000
	s_addc_u32 s55, s31, 0
	s_add_u32 s30, s30, 0x7000
	global_load_dwordx4 v[26:29], v240, s[54:55] offset:0
	s_addc_u32 s31, s31, 0
	global_load_dwordx4 v[30:33], v240, s[30:31] offset:0
	ds_write_b128 v210, v[194:197]
	ds_write_b128 v211, v[198:201]
	ds_write_b128 v212, v[202:205]
	ds_write_b128 v213, v[206:209]
	ds_read_b128 v[218:221], v248 offset:16384
	ds_read_b128 v[222:225], v248 offset:17408
	ds_read_b128 v[210:213], v248 offset:18432
	ds_read_b128 v[214:217], v248 offset:19456
	ds_read_b128 v[202:205], v248 offset:20480
	ds_read_b128 v[206:209], v248 offset:21504
	ds_read_b128 v[194:197], v248 offset:22528
	ds_read_b128 v[198:201], v248 offset:23552
	s_and_b64 s[30:31], s[28:29], exec
	s_cselect_b32 s2, 0, s2
	s_cselect_b32 s3, 0, 0
	s_add_u32 s30, s56, s2
	s_mov_b32 m0, s37
	s_addc_u32 s31, s57, s3
	global_load_lds_dwordx4 v226, s[30:31]
	s_mov_b32 m0, s38
	v_mov_b32_e32 v227, v231
	global_load_lds_dwordx4 v228, s[30:31]
	s_waitcnt vmcnt(12)
	s_waitcnt lgkmcnt(0)
	v_lshl_add_u64 v[238:239], s[30:31], 0, v[226:227]
	v_mov_b32_e32 v229, v231
	v_cndmask_b32_e64 v227, 0, 1, s[24:25]
	v_lshl_add_u64 v[236:237], s[30:31], 0, v[228:229]
	v_cmp_ne_u32_e64 s[2:3], 1, v227
	s_andn2_b64 vcc, exec, s[24:25]
	s_barrier
; #define PG8_STAGE_A(bufoff, V0, V1, kb) do { \
;         __builtin_amdgcn_global_load_lds((const unsigned*)((Abase + (kb)) + (V0)), (LAS unsigned*)(lds + (bufoff) + ldsw), 16, 0, 0); \
;         __builtin_amdgcn_global_load_lds((const unsigned*)((Abase + (kb)) + (V1)), (LAS unsigned*)(lds + (bufoff) + ldsw + 8192), 16, 0, 0); } while (0)
; #define PG8_LDA(dst, b, h) do { _Pragma("unroll") for (int m = 0; m < 4; ++m) _Pragma("unroll") for (int k = 0; k < 2; ++k) dst[m][k] = *(const LAS bf16x8*)(lds + PG8_SA(b, h) + aoff + m * 2048 + k * 1024); } while (0)
; #define PG8_LDB(dst, b, h) do { _Pragma("unroll") for (int n = 0; n < 2; ++n) _Pragma("unroll") for (int k = 0; k < 2; ++k) dst[n][k] = *(const LAS bf16x8*)(lds + PG8_SB(b, h) + boff + n * 2048 + k * 1024); } while (0)
; #define PG8_MMA(ai, bj, At, Bt) do { __builtin_amdgcn_s_setprio(1); _Pragma("unroll") for (int m = 0; m < 4; ++m) _Pragma("unroll") for (int n = 0; n < 2; ++n) _Pragma("unroll") for (int k = 0; k < 2; ++k) \
;         acc[ai][bj][m][n] = __builtin_amdgcn_mfma_f32_16x16x32_bf16(Bt[n][k], At[m][k], acc[ai][bj][m][n], 0, 0, 0); __builtin_amdgcn_s_setprio(0); } while (0)
; #define PG8_WAIT_V(n) asm volatile("s_waitcnt vmcnt(" #n ")" ::: "memory")
; #define PG8_WAIT_L(n) asm volatile("s_waitcnt lgkmcnt(" #n ")" ::: "memory")
; #define PG8_BAR __builtin_amdgcn_s_barrier()
; #define PG8_SCHED __builtin_amdgcn_sched_barrier(0)
; template <class Epi, class Sched, bool ALIGN_EPI>
; __device__ __forceinline__ void gemm_phase(LAS unsigned char* lds, const Gemm g, const Sched& S, const Epi& E) {
;     ...
;             PG8_WAIT_V(12); PG8_WAIT_L(0); PG8_BAR; if (half1) { PG8_MMA(1, 0, At, B0); PG8_MMA(1, 1, At, B1); } PG8_BAR; PG8_SCHED;
;             PG8_LDB(B0, 1, 0); PG8_LDB(B1, 1, 1); PG8_SCHED; PG8_LDA(At, 1, 0); PG8_STAGE_A(PG8_SA(0, 1), vc10, vc11, kb2);
;             PG8_WAIT_V(12); PG8_WAIT_L(0); PG8_BAR; PG8_MMA(0, 0, At, B0); PG8_MMA(0, 1, At, B1); PG8_BAR; PG8_SCHED;
	s_cbranch_vccnz .LBB0_4910
	s_setprio 1
	s_waitcnt lgkmcnt(0)
	v_mfma_f32_16x16x32_bf16 v[94:97], v[178:181], v[218:221], v[94:97]
	v_mfma_f32_16x16x32_bf16 v[90:93], v[186:189], v[218:221], v[90:93]
	v_mfma_f32_16x16x32_bf16 v[78:81], v[178:181], v[210:213], v[78:81]
	v_mfma_f32_16x16x32_bf16 v[74:77], v[186:189], v[210:213], v[74:77]
	v_mfma_f32_16x16x32_bf16 v[62:65], v[178:181], v[202:205], v[62:65]
	v_mfma_f32_16x16x32_bf16 v[58:61], v[186:189], v[202:205], v[58:61]
	v_mfma_f32_16x16x32_bf16 v[46:49], v[178:181], v[194:197], v[46:49]
	v_mfma_f32_16x16x32_bf16 v[42:45], v[186:189], v[194:197], v[42:45]
	v_mfma_f32_16x16x32_bf16 v[94:97], v[182:185], v[222:225], v[94:97]
	v_mfma_f32_16x16x32_bf16 v[90:93], v[190:193], v[222:225], v[90:93]
	v_mfma_f32_16x16x32_bf16 v[78:81], v[182:185], v[214:217], v[78:81]
	v_mfma_f32_16x16x32_bf16 v[74:77], v[190:193], v[214:217], v[74:77]
	v_mfma_f32_16x16x32_bf16 v[62:65], v[182:185], v[206:209], v[62:65]
	v_mfma_f32_16x16x32_bf16 v[58:61], v[190:193], v[206:209], v[58:61]
	v_mfma_f32_16x16x32_bf16 v[46:49], v[182:185], v[198:201], v[46:49]
	v_mfma_f32_16x16x32_bf16 v[42:45], v[190:193], v[198:201], v[42:45]
	s_setprio 0
	s_setprio 1
	v_mfma_f32_16x16x32_bf16 v[86:89], v[162:165], v[218:221], v[86:89]
	v_mfma_f32_16x16x32_bf16 v[82:85], v[170:173], v[218:221], v[82:85]
	v_mfma_f32_16x16x32_bf16 v[70:73], v[162:165], v[210:213], v[70:73]
	v_mfma_f32_16x16x32_bf16 v[66:69], v[170:173], v[210:213], v[66:69]
	v_mfma_f32_16x16x32_bf16 v[54:57], v[162:165], v[202:205], v[54:57]
	v_mfma_f32_16x16x32_bf16 v[50:53], v[170:173], v[202:205], v[50:53]
	v_mfma_f32_16x16x32_bf16 v[38:41], v[162:165], v[194:197], v[38:41]
	v_mfma_f32_16x16x32_bf16 v[34:37], v[170:173], v[194:197], v[34:37]
	v_mfma_f32_16x16x32_bf16 v[86:89], v[166:169], v[222:225], v[86:89]
	v_mfma_f32_16x16x32_bf16 v[82:85], v[174:177], v[222:225], v[82:85]
	v_mfma_f32_16x16x32_bf16 v[70:73], v[166:169], v[214:217], v[70:73]
	v_mfma_f32_16x16x32_bf16 v[66:69], v[174:177], v[214:217], v[66:69]
	v_mfma_f32_16x16x32_bf16 v[54:57], v[166:169], v[206:209], v[54:57]
	v_mfma_f32_16x16x32_bf16 v[50:53], v[174:177], v[206:209], v[50:53]
	v_mfma_f32_16x16x32_bf16 v[38:41], v[166:169], v[198:201], v[38:41]
	v_mfma_f32_16x16x32_bf16 v[34:37], v[174:177], v[198:201], v[34:37]
	s_setprio 0
.LBB0_4910:
	v_cndmask_b32_e64 v232, v232, v252, s[28:29]
	v_cndmask_b32_e64 v230, v230, v251, s[28:29]
	s_barrier
	s_mov_b32 m0, s39
	s_nop 0
	global_load_lds_dwordx4 v230, s[30:31]
	s_mov_b32 m0, s40
	s_nop 0
	global_load_lds_dwordx4 v232, s[30:31]
	v_add_u32_e32 v162, 0x18000, v247
	v_add_u32_e32 v174, 0x1c000, v247
	ds_read_b128 v[178:181], v162
	ds_read_b128 v[182:185], v162 offset:1024
	ds_read_b128 v[186:189], v162 offset:2048
	ds_read_b128 v[190:193], v162 offset:3072
	ds_read_b128 v[162:165], v174
	ds_read_b128 v[166:169], v174 offset:1024
	ds_read_b128 v[170:173], v174 offset:2048
	ds_read_b128 v[174:177], v174 offset:3072
	s_waitcnt lgkmcnt(0)
	ds_read_b128 v[194:197], v248 offset:32768
	ds_read_b128 v[198:201], v248 offset:33792
	ds_read_b128 v[202:205], v248 offset:34816
	ds_read_b128 v[206:209], v248 offset:35840
	ds_read_b128 v[210:213], v248 offset:36864
	ds_read_b128 v[214:217], v248 offset:37888
	ds_read_b128 v[218:221], v248 offset:38912
	ds_read_b128 v[222:225], v248 offset:39936
	s_waitcnt vmcnt(12)
	s_waitcnt lgkmcnt(0)
	s_barrier
	s_setprio 1
	s_waitcnt lgkmcnt(0)
	v_mfma_f32_16x16x32_bf16 v[158:161], v[178:181], v[194:197], v[158:161]
	v_mfma_f32_16x16x32_bf16 v[154:157], v[186:189], v[194:197], v[154:157]
	v_mfma_f32_16x16x32_bf16 v[142:145], v[178:181], v[202:205], v[142:145]
	v_mfma_f32_16x16x32_bf16 v[138:141], v[186:189], v[202:205], v[138:141]
	v_mfma_f32_16x16x32_bf16 v[126:129], v[178:181], v[210:213], v[126:129]
	v_mfma_f32_16x16x32_bf16 v[122:125], v[186:189], v[210:213], v[122:125]
	v_mfma_f32_16x16x32_bf16 v[110:113], v[178:181], v[218:221], v[110:113]
	v_mfma_f32_16x16x32_bf16 v[106:109], v[186:189], v[218:221], v[106:109]
	v_mfma_f32_16x16x32_bf16 v[158:161], v[182:185], v[198:201], v[158:161]
	v_mfma_f32_16x16x32_bf16 v[154:157], v[190:193], v[198:201], v[154:157]
	v_mfma_f32_16x16x32_bf16 v[142:145], v[182:185], v[206:209], v[142:145]
	v_mfma_f32_16x16x32_bf16 v[138:141], v[190:193], v[206:209], v[138:141]
	v_mfma_f32_16x16x32_bf16 v[126:129], v[182:185], v[214:217], v[126:129]
	v_mfma_f32_16x16x32_bf16 v[122:125], v[190:193], v[214:217], v[122:125]
	v_mfma_f32_16x16x32_bf16 v[110:113], v[182:185], v[222:225], v[110:113]
	v_mfma_f32_16x16x32_bf16 v[106:109], v[190:193], v[222:225], v[106:109]
	s_setprio 0
	s_setprio 1
	v_mfma_f32_16x16x32_bf16 v[150:153], v[162:165], v[194:197], v[150:153]
	v_mfma_f32_16x16x32_bf16 v[146:149], v[170:173], v[194:197], v[146:149]
	v_mfma_f32_16x16x32_bf16 v[134:137], v[162:165], v[202:205], v[134:137]
	v_mfma_f32_16x16x32_bf16 v[130:133], v[170:173], v[202:205], v[130:133]
	v_mfma_f32_16x16x32_bf16 v[118:121], v[162:165], v[210:213], v[118:121]
	v_mfma_f32_16x16x32_bf16 v[114:117], v[170:173], v[210:213], v[114:117]
	v_mfma_f32_16x16x32_bf16 v[102:105], v[162:165], v[218:221], v[102:105]
	v_mfma_f32_16x16x32_bf16 v[98:101], v[170:173], v[218:221], v[98:101]
	v_mfma_f32_16x16x32_bf16 v[150:153], v[166:169], v[198:201], v[150:153]
	v_mfma_f32_16x16x32_bf16 v[146:149], v[174:177], v[198:201], v[146:149]
	v_mfma_f32_16x16x32_bf16 v[134:137], v[166:169], v[206:209], v[134:137]
	v_mfma_f32_16x16x32_bf16 v[130:133], v[174:177], v[206:209], v[130:133]
	v_mfma_f32_16x16x32_bf16 v[118:121], v[166:169], v[214:217], v[118:121]
	v_mfma_f32_16x16x32_bf16 v[114:117], v[174:177], v[214:217], v[114:117]
	v_mfma_f32_16x16x32_bf16 v[102:105], v[166:169], v[222:225], v[102:105]
	v_mfma_f32_16x16x32_bf16 v[98:101], v[174:177], v[222:225], v[98:101]
	s_setprio 0
	s_barrier
; #define PG8_BWAIT(n) asm volatile("s_waitcnt vmcnt(" #n ")" : "+v"(bv[0]), "+v"(bv[1]), "+v"(bv[2]), "+v"(bv[3]), "+v"(bv[4]), "+v"(bv[5]), "+v"(bv[6]), "+v"(bv[7]) :: "memory")
; #define PG8_STAGE_A(bufoff, V0, V1, kb) do { \
;         __builtin_amdgcn_global_load_lds((const unsigned*)((Abase + (kb)) + (V0)), (LAS unsigned*)(lds + (bufoff) + ldsw), 16, 0, 0); \
;         __builtin_amdgcn_global_load_lds((const unsigned*)((Abase + (kb)) + (V1)), (LAS unsigned*)(lds + (bufoff) + ldsw + 8192), 16, 0, 0); } while (0)
; #define PG8_LDA(dst, b, h) do { _Pragma("unroll") for (int m = 0; m < 4; ++m) _Pragma("unroll") for (int k = 0; k < 2; ++k) dst[m][k] = *(const LAS bf16x8*)(lds + PG8_SA(b, h) + aoff + m * 2048 + k * 1024); } while (0)
; #define PG8_MMA(ai, bj, At, Bt) do { __builtin_amdgcn_s_setprio(1); _Pragma("unroll") for (int m = 0; m < 4; ++m) _Pragma("unroll") for (int n = 0; n < 2; ++n) _Pragma("unroll") for (int k = 0; k < 2; ++k) \
;         acc[ai][bj][m][n] = __builtin_amdgcn_mfma_f32_16x16x32_bf16(Bt[n][k], At[m][k], acc[ai][bj][m][n], 0, 0, 0); __builtin_amdgcn_s_setprio(0); } while (0)
; #define PG8_WAIT_V(n) asm volatile("s_waitcnt vmcnt(" #n ")" ::: "memory")
; #define PG8_WAIT_L(n) asm volatile("s_waitcnt lgkmcnt(" #n ")" ::: "memory")
; #define PG8_BAR __builtin_amdgcn_s_barrier()
; #define PG8_SCHED __builtin_amdgcn_sched_barrier(0)
; template <class Epi, class Sched, bool ALIGN_EPI>
; __device__ __forceinline__ void gemm_phase(LAS unsigned char* lds, const Gemm g, const Sched& S, const Epi& E) {
;     ...
;             PG8_BWAIT(2); PG8_BCOMMIT(1); PG8_SCHED; PG8_LDA(At, 1, 1); PG8_BISSUE(t + 4 >= nt ? pbn + (size_t)(t + 4 - nt) * 64 * Sched::LDN : pbc + (size_t)(t + 4) * 64 * Sched::LDN); PG8_STAGE_A(PG8_SA(1, 0), vc00, vc01, kb2 + 128u);
;             PG8_WAIT_V(12); PG8_WAIT_L(0); PG8_BAR; if (half1) { PG8_MMA(1, 0, At, B0); PG8_MMA(1, 1, At, B1); } PG8_BAR; PG8_SCHED;
	s_waitcnt vmcnt(2)
	s_nop 0
	v_add_u32_e32 v210, 0x18000, v242
	v_cvt_pk_bf16_f32 v194, v2, v6
	v_cvt_pk_bf16_f32 v195, v10, v14
	v_cvt_pk_bf16_f32 v196, v18, v22
	v_cvt_pk_bf16_f32 v197, v26, v30
	v_cvt_pk_bf16_f32 v198, v3, v7
	v_cvt_pk_bf16_f32 v199, v11, v15
	v_cvt_pk_bf16_f32 v200, v19, v23
	v_cvt_pk_bf16_f32 v201, v27, v31
	v_cvt_pk_bf16_f32 v202, v4, v8
	v_cvt_pk_bf16_f32 v203, v12, v16
	v_cvt_pk_bf16_f32 v204, v20, v24
	v_cvt_pk_bf16_f32 v205, v28, v32
	v_cvt_pk_bf16_f32 v206, v5, v9
	v_cvt_pk_bf16_f32 v207, v13, v17
	v_cvt_pk_bf16_f32 v208, v21, v25
	v_cvt_pk_bf16_f32 v209, v29, v33
	v_xor_b32_e32 v211, 64, v210
	v_xor_b32_e32 v212, 0x80, v210
	v_xor_b32_e32 v213, 0xc0, v210
	s_lshl_b32 s8, s52, 16
	s_lshl_b64 s[28:29], s[8:9], 2
	s_add_u32 s28, s49, s28
	s_addc_u32 s29, s21, s29
	s_add_u32 s30, s28, 0x1000
	global_load_dwordx4 v[2:5], v240, s[28:29] offset:0
	s_addc_u32 s31, s29, 0
	global_load_dwordx4 v[6:9], v240, s[30:31] offset:0
	s_add_u32 s30, s28, 0x2000
	s_addc_u32 s31, s29, 0
	global_load_dwordx4 v[10:13], v240, s[30:31] offset:0
	s_add_u32 s30, s28, 0x3000
	s_addc_u32 s31, s29, 0
	global_load_dwordx4 v[14:17], v240, s[30:31] offset:0
	s_add_u32 s30, s28, 0x4000
	s_addc_u32 s31, s29, 0
	global_load_dwordx4 v[18:21], v240, s[30:31] offset:0
	s_add_u32 s30, s28, 0x5000
	s_addc_u32 s31, s29, 0
	global_load_dwordx4 v[22:25], v240, s[30:31] offset:0
	s_add_u32 s30, s28, 0x6000
	s_addc_u32 s31, s29, 0
	global_load_dwordx4 v[26:29], v240, s[30:31] offset:0
	s_add_u32 s28, s28, 0x7000
	s_mov_b32 m0, s41
	s_addc_u32 s29, s29, 0
	global_load_dwordx4 v[30:33], v240, s[28:29] offset:0
	ds_write_b128 v210, v[194:197]
	ds_write_b128 v211, v[198:201]
	ds_write_b128 v212, v[202:205]
	ds_write_b128 v213, v[206:209]
	ds_read_b128 v[218:221], v248 offset:49152
	ds_read_b128 v[222:225], v248 offset:50176
	ds_read_b128 v[210:213], v248 offset:51200
	ds_read_b128 v[214:217], v248 offset:52224
	ds_read_b128 v[202:205], v248 offset:53248
	ds_read_b128 v[206:209], v248 offset:54272
	ds_read_b128 v[194:197], v248 offset:55296
	ds_read_b128 v[198:201], v248 offset:56320
	v_lshl_add_u64 v[238:239], v[238:239], 0, s[14:15]
	global_load_lds_dwordx4 v[238:239], off
	v_lshl_add_u64 v[236:237], v[236:237], 0, s[14:15]
	s_mov_b32 m0, s42
	s_and_b64 vcc, exec, s[2:3]
	global_load_lds_dwordx4 v[236:237], off
	s_waitcnt vmcnt(12)
	s_waitcnt lgkmcnt(0)
	s_barrier
	s_cbranch_vccnz .LBB0_4907
	s_setprio 1
	s_waitcnt lgkmcnt(0)
	v_mfma_f32_16x16x32_bf16 v[94:97], v[178:181], v[218:221], v[94:97]
	v_mfma_f32_16x16x32_bf16 v[90:93], v[186:189], v[218:221], v[90:93]
	v_mfma_f32_16x16x32_bf16 v[78:81], v[178:181], v[210:213], v[78:81]
	v_mfma_f32_16x16x32_bf16 v[74:77], v[186:189], v[210:213], v[74:77]
	v_mfma_f32_16x16x32_bf16 v[62:65], v[178:181], v[202:205], v[62:65]
	v_mfma_f32_16x16x32_bf16 v[58:61], v[186:189], v[202:205], v[58:61]
	v_mfma_f32_16x16x32_bf16 v[46:49], v[178:181], v[194:197], v[46:49]
	v_mfma_f32_16x16x32_bf16 v[42:45], v[186:189], v[194:197], v[42:45]
	v_mfma_f32_16x16x32_bf16 v[94:97], v[182:185], v[222:225], v[94:97]
	v_mfma_f32_16x16x32_bf16 v[90:93], v[190:193], v[222:225], v[90:93]
	v_mfma_f32_16x16x32_bf16 v[78:81], v[182:185], v[214:217], v[78:81]
	v_mfma_f32_16x16x32_bf16 v[74:77], v[190:193], v[214:217], v[74:77]
	v_mfma_f32_16x16x32_bf16 v[62:65], v[182:185], v[206:209], v[62:65]
	v_mfma_f32_16x16x32_bf16 v[58:61], v[190:193], v[206:209], v[58:61]
	v_mfma_f32_16x16x32_bf16 v[46:49], v[182:185], v[198:201], v[46:49]
	v_mfma_f32_16x16x32_bf16 v[42:45], v[190:193], v[198:201], v[42:45]
	s_setprio 0
	s_setprio 1
	v_mfma_f32_16x16x32_bf16 v[86:89], v[162:165], v[218:221], v[86:89]
	v_mfma_f32_16x16x32_bf16 v[82:85], v[170:173], v[218:221], v[82:85]
	v_mfma_f32_16x16x32_bf16 v[70:73], v[162:165], v[210:213], v[70:73]
	v_mfma_f32_16x16x32_bf16 v[66:69], v[170:173], v[210:213], v[66:69]
	v_mfma_f32_16x16x32_bf16 v[54:57], v[162:165], v[202:205], v[54:57]
	v_mfma_f32_16x16x32_bf16 v[50:53], v[170:173], v[202:205], v[50:53]
	v_mfma_f32_16x16x32_bf16 v[38:41], v[162:165], v[194:197], v[38:41]
	v_mfma_f32_16x16x32_bf16 v[34:37], v[170:173], v[194:197], v[34:37]
	v_mfma_f32_16x16x32_bf16 v[86:89], v[166:169], v[222:225], v[86:89]
	v_mfma_f32_16x16x32_bf16 v[82:85], v[174:177], v[222:225], v[82:85]
	v_mfma_f32_16x16x32_bf16 v[70:73], v[166:169], v[214:217], v[70:73]
	v_mfma_f32_16x16x32_bf16 v[66:69], v[174:177], v[214:217], v[66:69]
	v_mfma_f32_16x16x32_bf16 v[54:57], v[166:169], v[206:209], v[54:57]
	v_mfma_f32_16x16x32_bf16 v[50:53], v[174:177], v[206:209], v[50:53]
	v_mfma_f32_16x16x32_bf16 v[38:41], v[166:169], v[198:201], v[38:41]
	v_mfma_f32_16x16x32_bf16 v[34:37], v[174:177], v[198:201], v[34:37]
	s_setprio 0
	s_branch .LBB0_4907
